# NA units: additionally skip P.V MFMAs and V tr-reads of tiles the wave found dead (P exactly 0)
# baseline (speedup 1.0000x reference)
.LBB0_610:
	s_add_i32 s20, s19, 2
	s_add_i32 s8, s12, s20
	v_cmp_ge_u32_e32 vcc, s8, v169
	v_cmp_lt_u32_e64 s[8:9], s8, v170
	s_nop 1
	s_and_b64 s[8:9], vcc, s[8:9]
	s_cmp_gt_u32 s20, 11
	s_cselect_b64 s[8:9], exec, s[8:9]
	s_cmp_eq_u64 s[8:9], 0
	s_cbranch_scc1 .Lna_deadA
	s_mov_b32 s100, 0
	ds_read_b128 v[64:67], v158 offset:49152
	ds_read_b128 v[240:243], v161 offset:49152
	ds_read_b128 v[244:247], v158 offset:57344
	ds_read_b128 v[248:251], v161 offset:57344
	v_add_f32_e32 v144, 0, v236
	v_add_f32_e32 v144, v238, v144
	v_add_f32_e32 v144, v145, v144
	v_add_f32_e32 v144, v237, v144
	v_add_f32_e32 v144, v146, v144
	v_add_f32_e32 v144, v235, v144
	v_add_f32_e32 v144, v147, v144
	v_add_f32_e32 v144, v234, v144
	v_add_f32_e32 v144, v231, v144
	v_add_f32_e32 v144, v233, v144
	v_add_f32_e32 v144, v230, v144
	v_add_f32_e32 v144, v232, v144
	v_exp_f32_e32 v134, v134
	v_add_f32_e32 v144, v227, v144
	v_exp_f32_e32 v135, v135
	v_add_f32_e32 v144, v229, v144
	v_exp_f32_e32 v138, v138
	v_add_f32_e32 v144, v226, v144
	v_exp_f32_e32 v139, v139
	v_add_f32_e32 v144, v228, v144
	v_exp_f32_e32 v130, v130
	v_add_f32_e32 v144, v134, v144
	v_exp_f32_e32 v131, v131
	v_add_f32_e32 v144, v135, v144
	v_exp_f32_e32 v132, v132
	v_add_f32_e32 v144, v138, v144
	v_exp_f32_e32 v133, v133
	v_add_f32_e32 v144, v139, v144
	v_exp_f32_e32 v136, v136
	v_add_f32_e32 v144, v130, v144
	v_exp_f32_e32 v137, v137
	v_add_f32_e32 v144, v131, v144
	v_exp_f32_e32 v142, v142
	v_add_f32_e32 v144, v132, v144
	v_exp_f32_e32 v143, v143
	v_add_f32_e32 v144, v133, v144
	v_exp_f32_e32 v140, v140
	v_add_f32_e32 v144, v136, v144
	v_exp_f32_e32 v141, v141
	v_add_f32_e32 v144, v137, v144
	v_exp_f32_e32 v128, v128
	v_add_f32_e32 v144, v142, v144
	v_exp_f32_e32 v129, v129
	v_add_f32_e32 v144, v143, v144
	v_add_f32_e32 v144, v140, v144
	v_add_f32_e32 v144, v141, v144
	v_add_f32_e32 v144, v128, v144
	v_add_f32_e32 v223, v129, v144
	v_mov_b32_e32 v224, v223
	v_cvt_pk_bf16_f32 v144, v236, v238
	v_cvt_pk_bf16_f32 v145, v145, v237
	v_cvt_pk_bf16_f32 v146, v146, v235
	s_nop 0
	v_permlane32_swap_b32_e32 v223, v224
	v_cvt_pk_bf16_f32 v147, v147, v234
	v_permlane32_swap_b32_e32 v144, v146
	v_cvt_pk_bf16_f32 v234, v231, v233
	v_cvt_pk_bf16_f32 v235, v230, v232
	v_cvt_pk_bf16_f32 v236, v227, v229
	v_cvt_pk_bf16_f32 v237, v226, v228
	v_cvt_pk_bf16_f32 v226, v134, v135
	v_cvt_pk_bf16_f32 v227, v138, v139
	v_cvt_pk_bf16_f32 v228, v130, v131
	v_cvt_pk_bf16_f32 v229, v132, v133
	v_cvt_pk_bf16_f32 v230, v136, v137
	v_cvt_pk_bf16_f32 v231, v142, v143
	v_cvt_pk_bf16_f32 v232, v140, v141
	v_cvt_pk_bf16_f32 v233, v128, v129
	v_permlane32_swap_b32_e32 v145, v147
	v_permlane32_swap_b32_e32 v234, v236
	v_permlane32_swap_b32_e32 v235, v237
	v_permlane32_swap_b32_e32 v226, v228
	v_permlane32_swap_b32_e32 v227, v229
	v_permlane32_swap_b32_e32 v230, v232
	v_permlane32_swap_b32_e32 v231, v233
	s_add_i32 s8, s19, 3
	s_cmp_lt_u32 s8, 12
	s_cselect_b64 s[10:11], -1, 0
	s_and_b64 s[8:9], s[10:11], exec
	s_cselect_b32 s8, 0, -12
	s_cselect_b32 s9, s13, 0x4000
	s_add_i32 s8, s8, s19
	s_lshl_b32 s8, s8, 6
	s_add_i32 s8, s8, s9
	s_mulk_i32 s8, 0x2400
	s_add_i32 s21, s8, 0x1b0000
	s_add_u32 s8, s14, s21
	s_addc_u32 s9, s15, 0
	s_add_u32 vcc_lo, s16, s21
	s_addc_u32 vcc_hi, s17, 0
	v_lshl_add_u64 v[128:129], vcc, 0, v[192:193]
	v_lshl_add_u64 v[132:133], vcc, 0, v[150:151]
	v_lshl_add_u64 v[136:137], s[8:9], 0, v[192:193]
	v_lshl_add_u64 v[140:141], s[8:9], 0, v[150:151]
	global_load_dwordx4 v[128:131], v[128:129], off
	s_nop 0
	global_load_dwordx4 v[132:135], v[132:133], off
	s_nop 0
	global_load_dwordx4 v[136:139], v[136:137], off
	s_nop 0
	global_load_dwordx4 v[140:143], v[140:141], off
	s_cmp_gt_u32 s20, 11
	s_waitcnt lgkmcnt(3)
	v_mfma_f32_32x32x16_bf16 v[80:95], v[64:67], v[100:103], 0
	s_waitcnt lgkmcnt(2)
	v_mfma_f32_32x32x16_bf16 v[80:95], v[240:243], v[104:107], v[80:95]
	ds_read_b128 v[240:243], v162 offset:49152
	s_waitcnt lgkmcnt(2)
	v_mfma_f32_32x32x16_bf16 v[64:79], v[244:247], v[100:103], 0
	ds_read_b128 v[244:247], v162 offset:57344
	s_waitcnt lgkmcnt(2)
	v_mfma_f32_32x32x16_bf16 v[64:79], v[248:251], v[104:107], v[64:79]
	ds_read_b128 v[248:251], v160 offset:49152
	s_waitcnt lgkmcnt(2)
	v_mfma_f32_32x32x16_bf16 v[80:95], v[240:243], v[120:123], v[80:95]
	ds_read_b128 v[240:243], v160 offset:57344
	s_waitcnt lgkmcnt(2)
	v_mfma_f32_32x32x16_bf16 v[64:79], v[244:247], v[120:123], v[64:79]
	ds_read_b128 v[244:247], v166 offset:49152
	s_waitcnt lgkmcnt(2)
	v_mfma_f32_32x32x16_bf16 v[80:95], v[248:251], v[124:127], v[80:95]
	ds_read_b128 v[248:251], v166 offset:57344
	s_waitcnt lgkmcnt(2)
	v_mfma_f32_32x32x16_bf16 v[64:79], v[240:243], v[124:127], v[64:79]
	ds_read_b128 v[240:243], v165 offset:49152
	s_waitcnt lgkmcnt(2)
	v_mfma_f32_32x32x16_bf16 v[80:95], v[244:247], v[116:119], v[80:95]
	ds_read_b128 v[244:247], v165 offset:57344
	s_waitcnt lgkmcnt(2)
	v_mfma_f32_32x32x16_bf16 v[64:79], v[248:251], v[116:119], v[64:79]
	ds_read_b128 v[248:251], v164 offset:49152
	s_waitcnt lgkmcnt(2)
	v_mfma_f32_32x32x16_bf16 v[80:95], v[240:243], v[112:115], v[80:95]
	ds_read_b128 v[240:243], v164 offset:57344
	s_waitcnt lgkmcnt(2)
	v_mfma_f32_32x32x16_bf16 v[64:79], v[244:247], v[112:115], v[64:79]
	ds_read_b128 v[244:247], v163 offset:49152
	s_waitcnt lgkmcnt(2)
	v_mfma_f32_32x32x16_bf16 v[80:95], v[248:251], v[108:111], v[80:95]
	ds_read_b128 v[248:251], v163 offset:57344
	s_waitcnt lgkmcnt(2)
	v_mfma_f32_32x32x16_bf16 v[64:79], v[240:243], v[108:111], v[64:79]
	s_waitcnt lgkmcnt(1)
	v_mfma_f32_32x32x16_bf16 v[80:95], v[244:247], v[96:99], v[80:95]
	s_waitcnt lgkmcnt(0)
	v_mfma_f32_32x32x16_bf16 v[64:79], v[248:251], v[96:99], v[64:79]
	s_cbranch_scc1 .LBB0_612
	v_add3_u32 v219, v215, s19, 2
	v_max_i32_e32 v219, -7, v219
	v_add_u32_e32 v219, 7, v219
	s_add_i32 s8, s12, s19
	v_min_u32_e32 v219, 14, v219
	s_add_i32 s8, s8, 2
	v_mul_u32_u24_e32 v219, 31, v219
	v_cmp_ge_u32_e32 vcc, s8, v169
	v_cmp_lt_u32_e64 s[8:9], s8, v170
	v_sub_u32_e32 v219, v219, v168
	s_and_b64 s[8:9], vcc, s[8:9]
	v_add_u32_e32 v219, 15, v219
	v_mov_b32_e32 v218, 0x1d1
	v_add_u32_e32 v239, v219, v173
	s_and_b64 vcc, s[36:37], s[8:9]
	v_cndmask_b32_e32 v239, v218, v239, vcc
	v_lshl_add_u32 v239, v239, 2, s18
	ds_read_b32 v239, v239
	v_readlane_b32 s10, v255, 28
	v_readlane_b32 s11, v255, 29
	v_readlane_b32 s22, v255, 30
	s_and_b64 s[10:11], s[8:9], s[10:11]
	v_add_u32_e32 v240, v219, v174
	s_and_b64 vcc, s[38:39], s[8:9]
	v_cndmask_b32_e32 v240, v218, v240, vcc
	v_lshl_add_u32 v240, v240, 2, s18
	ds_read_b32 v240, v240
	v_readlane_b32 s23, v255, 31
	v_add_u32_e32 v241, v219, v175
	s_and_b64 vcc, s[40:41], s[8:9]
	v_cndmask_b32_e32 v241, v218, v241, vcc
	v_lshl_add_u32 v241, v241, 2, s18
	ds_read_b32 v241, v241
	v_add_u32_e32 v242, v219, v176
	s_and_b64 vcc, s[42:43], s[8:9]
	v_cndmask_b32_e32 v242, v218, v242, vcc
	v_lshl_add_u32 v242, v242, 2, s18
	ds_read_b32 v242, v242
	v_add_u32_e32 v243, v219, v177
	s_and_b64 vcc, s[8:9], s[44:45]
	v_cndmask_b32_e32 v243, v218, v243, vcc
	v_lshl_add_u32 v243, v243, 2, s18
	ds_read_b32 v243, v243
	v_add_u32_e32 v244, v219, v178
	s_and_b64 vcc, s[8:9], s[46:47]
	v_cndmask_b32_e32 v244, v218, v244, vcc
	v_lshl_add_u32 v244, v244, 2, s18
	ds_read_b32 v244, v244
	v_add_u32_e32 v245, v219, v179
	s_and_b64 vcc, s[8:9], s[48:49]
	v_cndmask_b32_e32 v245, v218, v245, vcc
	v_lshl_add_u32 v245, v245, 2, s18
	ds_read_b32 v245, v245
	v_add_u32_e32 v246, v219, v180
	s_and_b64 vcc, s[8:9], s[50:51]
	v_cndmask_b32_e32 v246, v218, v246, vcc
	v_lshl_add_u32 v246, v246, 2, s18
	ds_read_b32 v246, v246
	v_add_u32_e32 v247, v219, v181
	s_and_b64 vcc, s[10:11], s[22:23]
	v_cndmask_b32_e32 v247, v218, v247, vcc
	v_lshl_add_u32 v247, v247, 2, s18
	ds_read_b32 v247, v247
	v_readlane_b32 s10, v255, 32
	v_readlane_b32 s11, v255, 33
	v_readlane_b32 s22, v255, 34
	s_and_b64 s[10:11], s[8:9], s[10:11]
	v_readlane_b32 s23, v255, 35
	v_add_u32_e32 v248, v219, v182
	s_and_b64 vcc, s[10:11], s[22:23]
	v_cndmask_b32_e32 v248, v218, v248, vcc
	v_lshl_add_u32 v248, v248, 2, s18
	ds_read_b32 v248, v248
	v_readlane_b32 s10, v255, 36
	v_readlane_b32 s11, v255, 37
	v_readlane_b32 s22, v255, 38
	s_and_b64 s[10:11], s[8:9], s[10:11]
	v_readlane_b32 s23, v255, 39
	v_add_u32_e32 v249, v219, v183
	s_and_b64 vcc, s[10:11], s[22:23]
	v_cndmask_b32_e32 v249, v218, v249, vcc
	v_lshl_add_u32 v249, v249, 2, s18
	ds_read_b32 v249, v249
	v_readlane_b32 s10, v255, 40
	v_readlane_b32 s11, v255, 41
	v_readlane_b32 s22, v255, 42
	s_and_b64 s[10:11], s[8:9], s[10:11]
	v_readlane_b32 s23, v255, 43
	v_add_u32_e32 v250, v219, v184
	s_and_b64 vcc, s[10:11], s[22:23]
	v_cndmask_b32_e32 v250, v218, v250, vcc
	v_lshl_add_u32 v250, v250, 2, s18
	ds_read_b32 v250, v250
	v_readlane_b32 s10, v255, 44
	v_readlane_b32 s11, v255, 45
	s_and_b64 s[10:11], s[8:9], s[10:11]
	v_add_u32_e32 v251, v219, v185
	s_and_b64 vcc, s[10:11], s[30:31]
	v_cndmask_b32_e32 v251, v218, v251, vcc
	v_lshl_add_u32 v251, v251, 2, s18
	ds_read_b32 v251, v251
	s_and_b64 s[10:11], s[8:9], s[34:35]
	v_add_u32_e32 v252, v219, v186
	s_and_b64 vcc, s[10:11], s[24:25]
	v_cndmask_b32_e32 v252, v218, v252, vcc
	v_lshl_add_u32 v252, v252, 2, s18
	ds_read_b32 v252, v252
	s_and_b64 s[10:11], s[8:9], s[26:27]
	v_add_u32_e32 v253, v219, v187
	s_and_b64 vcc, s[10:11], s[28:29]
	v_cndmask_b32_e32 v253, v218, v253, vcc
	v_lshl_add_u32 v253, v253, 2, s18
	ds_read_b32 v253, v253
	s_and_b64 s[10:11], s[8:9], s[52:53]
	s_waitcnt lgkmcnt(14)
	v_add_f32_e32 v80, v80, v239
	v_add_u32_e32 v239, v219, v188
	s_and_b64 vcc, s[10:11], s[54:55]
	v_cndmask_b32_e32 v239, v218, v239, vcc
	v_lshl_add_u32 v239, v239, 2, s18
	ds_read_b32 v239, v239
	s_and_b64 s[10:11], s[8:9], s[56:57]
	s_waitcnt lgkmcnt(14)
	v_add_f32_e32 v81, v81, v240
	v_add_u32_e32 v240, v219, v189
	s_and_b64 vcc, s[10:11], s[58:59]
	v_cndmask_b32_e32 v240, v218, v240, vcc
	v_lshl_add_u32 v240, v240, 2, s18
	ds_read_b32 v240, v240
	s_and_b64 s[10:11], s[8:9], s[60:61]
	s_waitcnt lgkmcnt(14)
	v_add_f32_e32 v82, v82, v241
	v_add_u32_e32 v241, v219, v190
	s_and_b64 vcc, s[10:11], s[62:63]
	v_cndmask_b32_e32 v241, v218, v241, vcc
	v_lshl_add_u32 v241, v241, 2, s18
	ds_read_b32 v241, v241
	s_and_b64 s[10:11], s[8:9], s[64:65]
	s_waitcnt lgkmcnt(14)
	v_add_f32_e32 v83, v83, v242
	v_add_u32_e32 v242, v219, v191
	s_and_b64 vcc, s[10:11], s[66:67]
	v_cndmask_b32_e32 v242, v218, v242, vcc
	v_lshl_add_u32 v242, v242, 2, s18
	ds_read_b32 v242, v242
	s_and_b64 s[10:11], s[8:9], s[68:69]
	s_waitcnt lgkmcnt(14)
	v_add_f32_e32 v84, v84, v243
	v_add_u32_e32 v243, v219, v200
	s_and_b64 vcc, s[10:11], s[70:71]
	v_cndmask_b32_e32 v243, v218, v243, vcc
	v_lshl_add_u32 v243, v243, 2, s18
	ds_read_b32 v243, v243
	s_and_b64 s[10:11], s[8:9], s[72:73]
	s_waitcnt lgkmcnt(14)
	v_add_f32_e32 v85, v85, v244
	v_add_u32_e32 v244, v219, v201
	s_and_b64 vcc, s[10:11], s[74:75]
	v_cndmask_b32_e32 v244, v218, v244, vcc
	v_lshl_add_u32 v244, v244, 2, s18
	ds_read_b32 v244, v244
	s_and_b64 s[10:11], s[8:9], s[76:77]
	s_waitcnt lgkmcnt(14)
	v_add_f32_e32 v86, v86, v245
	v_add_u32_e32 v245, v219, v203
	s_and_b64 vcc, s[10:11], s[78:79]
	v_cndmask_b32_e32 v245, v218, v245, vcc
	v_lshl_add_u32 v245, v245, 2, s18
	ds_read_b32 v245, v245
	s_and_b64 s[10:11], s[8:9], s[80:81]
	s_waitcnt lgkmcnt(14)
	v_add_f32_e32 v87, v87, v246
	v_add_u32_e32 v246, v219, v204
	s_and_b64 vcc, s[10:11], s[82:83]
	v_cndmask_b32_e32 v246, v218, v246, vcc
	v_lshl_add_u32 v246, v246, 2, s18
	ds_read_b32 v246, v246
	s_and_b64 s[10:11], s[8:9], s[84:85]
	s_waitcnt lgkmcnt(14)
	v_add_f32_e32 v88, v88, v247
	v_add_u32_e32 v247, v219, v205
	s_and_b64 vcc, s[10:11], s[86:87]
	v_cndmask_b32_e32 v247, v218, v247, vcc
	v_lshl_add_u32 v247, v247, 2, s18
	ds_read_b32 v247, v247
	s_waitcnt lgkmcnt(14)
	v_add_f32_e32 v89, v89, v248
	v_add_u32_e32 v248, v219, v206
	s_and_b64 vcc, s[8:9], s[88:89]
	v_cndmask_b32_e32 v248, v218, v248, vcc
	v_lshl_add_u32 v248, v248, 2, s18
	ds_read_b32 v248, v248
	s_waitcnt lgkmcnt(14)
	v_add_f32_e32 v90, v90, v249
	v_add_u32_e32 v249, v219, v207
	s_and_b64 vcc, s[8:9], s[90:91]
	v_cndmask_b32_e32 v249, v218, v249, vcc
	v_lshl_add_u32 v249, v249, 2, s18
	ds_read_b32 v249, v249
	s_waitcnt lgkmcnt(14)
	v_add_f32_e32 v91, v91, v250
	v_add_u32_e32 v250, v219, v208
	s_and_b64 vcc, s[8:9], s[92:93]
	v_cndmask_b32_e32 v250, v218, v250, vcc
	v_lshl_add_u32 v250, v250, 2, s18
	ds_read_b32 v250, v250
	s_waitcnt lgkmcnt(14)
	v_add_f32_e32 v92, v92, v251
	v_add_u32_e32 v251, v219, v209
	s_and_b64 vcc, s[8:9], s[94:95]
	v_cndmask_b32_e32 v251, v218, v251, vcc
	v_lshl_add_u32 v251, v251, 2, s18
	ds_read_b32 v251, v251
	s_waitcnt lgkmcnt(14)
	v_add_f32_e32 v93, v93, v252
	v_add_u32_e32 v252, v219, v210
	s_and_b64 vcc, s[8:9], s[96:97]
	v_cndmask_b32_e32 v252, v218, v252, vcc
	v_lshl_add_u32 v252, v252, 2, s18
	ds_read_b32 v252, v252
	s_waitcnt lgkmcnt(14)
	v_add_f32_e32 v94, v94, v253
	v_add_u32_e32 v253, v219, v211
	s_and_b64 vcc, s[8:9], s[2:3]
	v_cndmask_b32_e32 v253, v218, v253, vcc
	v_lshl_add_u32 v253, v253, 2, s18
	ds_read_b32 v253, v253
	s_waitcnt lgkmcnt(14)
	v_add_f32_e32 v95, v95, v239
	v_add_u32_e32 v239, v219, v212
	s_and_b64 vcc, s[8:9], s[0:1]
	v_cndmask_b32_e32 v239, v218, v239, vcc
	v_lshl_add_u32 v239, v239, 2, s18
	ds_read_b32 v239, v239
	s_waitcnt lgkmcnt(14)
	v_add_f32_e32 v64, v64, v240
	v_add_u32_e32 v240, v219, v213
	s_and_b64 vcc, s[8:9], s[6:7]
	v_cndmask_b32_e32 v240, v218, v240, vcc
	v_lshl_add_u32 v240, v240, 2, s18
	ds_read_b32 v240, v240
	s_waitcnt lgkmcnt(14)
	v_add_f32_e32 v65, v65, v241
	s_waitcnt lgkmcnt(13)
	v_add_f32_e32 v66, v66, v242
	s_waitcnt lgkmcnt(12)
	v_add_f32_e32 v67, v67, v243
	s_waitcnt lgkmcnt(11)
	v_add_f32_e32 v68, v68, v244
	s_waitcnt lgkmcnt(10)
	v_add_f32_e32 v69, v69, v245
	s_waitcnt lgkmcnt(9)
	v_add_f32_e32 v70, v70, v246
	s_waitcnt lgkmcnt(8)
	v_add_f32_e32 v71, v71, v247
	s_waitcnt lgkmcnt(7)
	v_add_f32_e32 v72, v72, v248
	s_waitcnt lgkmcnt(6)
	v_add_f32_e32 v73, v73, v249
	s_waitcnt lgkmcnt(5)
	v_add_f32_e32 v74, v74, v250
	s_waitcnt lgkmcnt(4)
	v_add_f32_e32 v75, v75, v251
	s_waitcnt lgkmcnt(3)
	v_add_f32_e32 v76, v76, v252
	s_waitcnt lgkmcnt(2)
	v_add_f32_e32 v77, v77, v253
	s_waitcnt lgkmcnt(1)
	v_add_f32_e32 v78, v78, v239
	s_waitcnt lgkmcnt(0)
	v_add_f32_e32 v79, v79, v240
.LBB0_612:
	s_add_i32 s8, s19, 3
	s_cmp_lt_u32 s8, 12
	s_cselect_b64 s[10:11], -1, 0
	s_cmp_eq_u32 s101, 1
	s_cbranch_scc1 .Lna_pvdB
	ds_read_b64_tr_b16 v[238:239], v202 offset:0
	ds_read_b64_tr_b16 v[240:241], v202 offset:0x800
	ds_read_b64_tr_b16 v[242:243], v202 offset:0x1000
	ds_read_b64_tr_b16 v[244:245], v202 offset:0x1800
	ds_read_b64_tr_b16 v[246:247], v202 offset:0x2000
	ds_read_b64_tr_b16 v[248:249], v202 offset:0x2800
	ds_read_b64_tr_b16 v[250:251], v202 offset:0x3000
	ds_read_b64_tr_b16 v[252:253], v202 offset:0x3800
	s_waitcnt lgkmcnt(0)
	s_nop 0
	v_mfma_f32_32x32x16_bf16 v[0:15], v[144:147], v[238:241], v[0:15]
	ds_read_b64_tr_b16 v[238:239], v202 offset:0x200
	ds_read_b64_tr_b16 v[240:241], v202 offset:0xa00
	v_mfma_f32_32x32x16_bf16 v[0:15], v[234:237], v[242:245], v[0:15]
	ds_read_b64_tr_b16 v[242:243], v202 offset:0x1200
	ds_read_b64_tr_b16 v[244:245], v202 offset:0x1a00
	v_mfma_f32_32x32x16_bf16 v[0:15], v[226:229], v[246:249], v[0:15]
	ds_read_b64_tr_b16 v[246:247], v202 offset:0x2200
	ds_read_b64_tr_b16 v[248:249], v202 offset:0x2a00
	v_mfma_f32_32x32x16_bf16 v[0:15], v[230:233], v[250:253], v[0:15]
	ds_read_b64_tr_b16 v[250:251], v202 offset:0x3200
	ds_read_b64_tr_b16 v[252:253], v202 offset:0x3a00
	s_waitcnt lgkmcnt(0)
	v_mfma_f32_32x32x16_bf16 v[48:63], v[144:147], v[238:241], v[48:63]
	ds_read_b64_tr_b16 v[238:239], v202 offset:0x400
	ds_read_b64_tr_b16 v[240:241], v202 offset:0xc00
	v_mfma_f32_32x32x16_bf16 v[48:63], v[234:237], v[242:245], v[48:63]
	ds_read_b64_tr_b16 v[242:243], v202 offset:0x1400
	ds_read_b64_tr_b16 v[244:245], v202 offset:0x1c00
	v_mfma_f32_32x32x16_bf16 v[48:63], v[226:229], v[246:249], v[48:63]
	ds_read_b64_tr_b16 v[246:247], v202 offset:0x2400
	ds_read_b64_tr_b16 v[248:249], v202 offset:0x2c00
	v_mfma_f32_32x32x16_bf16 v[48:63], v[230:233], v[250:253], v[48:63]
	ds_read_b64_tr_b16 v[250:251], v202 offset:0x3400
	ds_read_b64_tr_b16 v[252:253], v202 offset:0x3c00
	s_waitcnt lgkmcnt(0)
	v_mfma_f32_32x32x16_bf16 v[32:47], v[144:147], v[238:241], v[32:47]
	ds_read_b64_tr_b16 v[238:239], v202 offset:0x600
	ds_read_b64_tr_b16 v[240:241], v202 offset:0xe00
	v_mfma_f32_32x32x16_bf16 v[32:47], v[234:237], v[242:245], v[32:47]
	ds_read_b64_tr_b16 v[242:243], v202 offset:0x1600
	ds_read_b64_tr_b16 v[244:245], v202 offset:0x1e00
	v_mfma_f32_32x32x16_bf16 v[32:47], v[226:229], v[246:249], v[32:47]
	ds_read_b64_tr_b16 v[246:247], v202 offset:0x2600
	ds_read_b64_tr_b16 v[248:249], v202 offset:0x2e00
	v_mfma_f32_32x32x16_bf16 v[32:47], v[230:233], v[250:253], v[32:47]
	ds_read_b64_tr_b16 v[250:251], v202 offset:0x3600
	ds_read_b64_tr_b16 v[252:253], v202 offset:0x3e00
	s_waitcnt lgkmcnt(0)
	v_mfma_f32_32x32x16_bf16 v[16:31], v[144:147], v[238:241], v[16:31]
	v_max_f32_e32 v144, v81, v81
	v_max_f32_e32 v145, v80, v80
	v_max_f32_e32 v144, v145, v144
	v_max3_f32 v144, v144, v82, v83
	v_max3_f32 v144, v144, v84, v85
	v_max3_f32 v144, v144, v86, v87
	v_max3_f32 v144, v144, v88, v89
	v_max3_f32 v144, v144, v90, v91
	v_max3_f32 v144, v144, v92, v93
	v_mfma_f32_32x32x16_bf16 v[16:31], v[234:237], v[242:245], v[16:31]
	v_max3_f32 v144, v144, v94, v95
	v_max3_f32 v144, v144, v64, v65
	v_max3_f32 v144, v144, v66, v67
	v_max3_f32 v144, v144, v68, v69
	v_max3_f32 v144, v144, v70, v71
	v_max3_f32 v144, v144, v72, v73
	v_max3_f32 v144, v144, v74, v75
	v_max3_f32 v144, v144, v76, v77
	v_mfma_f32_32x32x16_bf16 v[16:31], v[226:229], v[246:249], v[16:31]
	v_max3_f32 v144, v144, v78, v79
	v_mov_b32_e32 v145, v144
	s_nop 1
	v_permlane32_swap_b32_e32 v144, v145
	v_max_f32_e32 v145, v145, v145
	v_max_f32_e32 v144, v144, v144
	v_max_f32_e32 v144, v144, v145
	v_sub_f32_e32 v145, v144, v222
	s_mov_b32 s8, 0x42b504f3
	v_cmp_ge_f32_e32 vcc, s8, v145
	v_max_f32_e32 v145, v222, v222
	v_max_f32_e32 v144, v145, v144
	v_mfma_f32_32x32x16_bf16 v[16:31], v[230:233], v[250:253], v[16:31]
	v_sub_f32_e32 v145, v222, v144
	v_mul_f32_e32 v145, 0x3e0293ee, v145
	v_exp_f32_e32 v145, v145
	s_cmp_eq_u64 vcc, exec
	s_cselect_b64 s[8:9], -1, 0
.Lna_pvjB:
	s_barrier
	s_waitcnt vmcnt(0)
	v_cndmask_b32_e64 v225, v145, 1.0, s[8:9]
	v_cmp_gt_f32_e32 vcc, 1.0, v225
	s_waitcnt vmcnt(3)
	ds_write_b128 v156, v[128:131]
	s_waitcnt vmcnt(2)
	ds_write_b128 v157, v[132:135]
	s_waitcnt vmcnt(1)
	ds_write_b128 v153, v[136:139] offset:32768
	s_waitcnt vmcnt(0)
	ds_write_b128 v155, v[140:143] offset:32768
	s_cbranch_vccz .LBB0_616
	s_and_saveexec_b64 vcc, s[4:5]
	ds_write_b32 v171, v225 offset:128
	s_or_b64 exec, exec, vcc
	s_waitcnt lgkmcnt(0)
	v_add_u32_e32 v140, v159, v148
	ds_read_b128 v[128:131], v140 offset:224
	ds_read_b128 v[132:135], v140 offset:192
	ds_read_b128 v[136:139], v140 offset:160
	ds_read_b128 v[140:143], v140 offset:128
	s_waitcnt lgkmcnt(3)
	v_pk_mul_f32 v[12:13], v[12:13], v[128:129]
	s_waitcnt lgkmcnt(2)
	v_pk_mul_f32 v[8:9], v[8:9], v[132:133]
	s_waitcnt lgkmcnt(1)
	v_pk_mul_f32 v[4:5], v[4:5], v[136:137]
	v_pk_mul_f32 v[14:15], v[14:15], v[130:131]
	v_pk_mul_f32 v[10:11], v[10:11], v[134:135]
	v_pk_mul_f32 v[6:7], v[6:7], v[138:139]
	s_waitcnt lgkmcnt(0)
	v_pk_mul_f32 v[2:3], v[2:3], v[142:143]
	v_pk_mul_f32 v[0:1], v[0:1], v[140:141]
	v_pk_mul_f32 v[60:61], v[60:61], v[128:129]
	v_pk_mul_f32 v[56:57], v[56:57], v[132:133]
	v_pk_mul_f32 v[52:53], v[52:53], v[136:137]
	v_pk_mul_f32 v[62:63], v[62:63], v[130:131]
	v_pk_mul_f32 v[58:59], v[58:59], v[134:135]
	v_pk_mul_f32 v[54:55], v[54:55], v[138:139]
	v_pk_mul_f32 v[50:51], v[50:51], v[142:143]
	v_pk_mul_f32 v[48:49], v[48:49], v[140:141]
	v_pk_mul_f32 v[44:45], v[44:45], v[128:129]
	v_pk_mul_f32 v[40:41], v[40:41], v[132:133]
	v_pk_mul_f32 v[36:37], v[36:37], v[136:137]
	v_pk_mul_f32 v[46:47], v[46:47], v[130:131]
	v_pk_mul_f32 v[42:43], v[42:43], v[134:135]
	v_pk_mul_f32 v[38:39], v[38:39], v[138:139]
	v_pk_mul_f32 v[34:35], v[34:35], v[142:143]
	v_pk_mul_f32 v[32:33], v[32:33], v[140:141]
	v_pk_mul_f32 v[28:29], v[28:29], v[128:129]
	v_pk_mul_f32 v[24:25], v[24:25], v[132:133]
	v_pk_mul_f32 v[20:21], v[20:21], v[136:137]
	v_pk_mul_f32 v[30:31], v[30:31], v[130:131]
	v_pk_mul_f32 v[26:27], v[26:27], v[134:135]
	v_pk_mul_f32 v[22:23], v[22:23], v[138:139]
	v_pk_mul_f32 v[18:19], v[18:19], v[142:143]
	v_pk_mul_f32 v[16:17], v[16:17], v[140:141]
.LBB0_616:
	v_cndmask_b32_e64 v222, v144, v222, s[8:9]
	v_mul_f32_e32 v144, 0xbe0293ee, v222
	v_fmamk_f32 v80, v80, 0x3e0293ee, v144
	v_fmamk_f32 v81, v81, 0x3e0293ee, v144
	v_fmamk_f32 v82, v82, 0x3e0293ee, v144
	v_fmamk_f32 v83, v83, 0x3e0293ee, v144
	v_fmamk_f32 v84, v84, 0x3e0293ee, v144
	v_fmamk_f32 v85, v85, 0x3e0293ee, v144
	v_fmamk_f32 v86, v86, 0x3e0293ee, v144
	v_fmamk_f32 v87, v87, 0x3e0293ee, v144
	v_fmamk_f32 v88, v88, 0x3e0293ee, v144
	v_fmamk_f32 v89, v89, 0x3e0293ee, v144
	v_fmamk_f32 v90, v90, 0x3e0293ee, v144
	v_fmamk_f32 v91, v91, 0x3e0293ee, v144
	v_fmamk_f32 v92, v92, 0x3e0293ee, v144
	v_fmamk_f32 v93, v93, 0x3e0293ee, v144
	v_fmamk_f32 v94, v94, 0x3e0293ee, v144
	v_fmamk_f32 v95, v95, 0x3e0293ee, v144
	v_exp_f32_e32 v141, v80
	v_exp_f32_e32 v143, v81
	v_exp_f32_e32 v139, v82
	v_exp_f32_e32 v142, v83
	v_exp_f32_e32 v137, v84
	v_exp_f32_e32 v140, v85
	v_exp_f32_e32 v136, v86
	v_exp_f32_e32 v138, v87
	v_exp_f32_e32 v133, v88
	v_exp_f32_e32 v135, v89
	v_exp_f32_e32 v131, v90
	v_exp_f32_e32 v134, v91
	v_exp_f32_e32 v129, v92
	v_exp_f32_e32 v132, v93
	v_exp_f32_e32 v128, v94
	v_exp_f32_e32 v130, v95
	v_fmamk_f32 v145, v64, 0x3e0293ee, v144
	v_fmamk_f32 v146, v65, 0x3e0293ee, v144
	v_fmamk_f32 v147, v66, 0x3e0293ee, v144
	v_fmamk_f32 v226, v67, 0x3e0293ee, v144
	v_fmamk_f32 v227, v68, 0x3e0293ee, v144
	v_fmamk_f32 v228, v69, 0x3e0293ee, v144
	v_fmamk_f32 v229, v70, 0x3e0293ee, v144
	v_fmamk_f32 v230, v71, 0x3e0293ee, v144
	v_fmamk_f32 v231, v72, 0x3e0293ee, v144
	v_fmamk_f32 v232, v73, 0x3e0293ee, v144
	v_fmamk_f32 v233, v74, 0x3e0293ee, v144
	v_fmamk_f32 v234, v75, 0x3e0293ee, v144
	v_fmamk_f32 v235, v76, 0x3e0293ee, v144
	v_fmamk_f32 v236, v77, 0x3e0293ee, v144
	v_fmamk_f32 v237, v78, 0x3e0293ee, v144
	v_fmac_f32_e32 v144, 0x3e0293ee, v79
	s_waitcnt lgkmcnt(0)
	s_barrier
	s_add_i32 s8, s12, s19
	s_add_i32 s8, s8, 3
	v_cmp_ge_u32_e32 vcc, s8, v169
	v_cmp_lt_u32_e64 s[8:9], s8, v170
	s_nop 1
	s_and_b64 s[8:9], vcc, s[8:9]
	s_andn2_b64 s[22:23], exec, s[10:11]
	s_or_b64 s[8:9], s[8:9], s[22:23]
	s_cmp_eq_u64 s[8:9], 0
	s_cbranch_scc1 .Lna_deadB
	s_mov_b32 s101, 0
	ds_read_b128 v[64:67], v158 offset:32768
	ds_read_b128 v[250:253], v161 offset:32768
	s_andn2_b64 vcc, exec, s[10:11]
	v_exp_f32_e32 v249, v144
	v_add_f32_e32 v144, 0, v141
	v_add_f32_e32 v144, v143, v144
	v_add_f32_e32 v144, v139, v144
	v_add_f32_e32 v144, v142, v144
	v_add_f32_e32 v144, v137, v144
	v_add_f32_e32 v144, v140, v144
	v_add_f32_e32 v144, v136, v144
	v_add_f32_e32 v144, v138, v144
	v_add_f32_e32 v144, v133, v144
	v_add_f32_e32 v144, v135, v144
	v_add_f32_e32 v144, v131, v144
	v_add_f32_e32 v144, v134, v144
	v_exp_f32_e32 v218, v145
	v_add_f32_e32 v144, v129, v144
	v_exp_f32_e32 v219, v146
	v_add_f32_e32 v144, v132, v144
	v_exp_f32_e32 v220, v147
	v_add_f32_e32 v144, v128, v144
	v_exp_f32_e32 v221, v226
	v_add_f32_e32 v144, v130, v144
	v_exp_f32_e32 v238, v227
	v_add_f32_e32 v144, v218, v144
	v_exp_f32_e32 v241, v228
	v_add_f32_e32 v144, v219, v144
	v_exp_f32_e32 v242, v229
	v_add_f32_e32 v144, v220, v144
	v_exp_f32_e32 v243, v230
	v_add_f32_e32 v144, v221, v144
	v_exp_f32_e32 v244, v231
	v_add_f32_e32 v144, v238, v144
	v_exp_f32_e32 v245, v232
	v_add_f32_e32 v144, v241, v144
	v_exp_f32_e32 v246, v233
	v_add_f32_e32 v144, v242, v144
	v_exp_f32_e32 v247, v234
	v_add_f32_e32 v144, v243, v144
	v_exp_f32_e32 v248, v235
	v_add_f32_e32 v144, v244, v144
	v_exp_f32_e32 v236, v236
	v_add_f32_e32 v144, v245, v144
	v_exp_f32_e32 v237, v237
	v_add_f32_e32 v144, v246, v144
	v_add_f32_e32 v144, v247, v144
	v_add_f32_e32 v144, v248, v144
	v_add_f32_e32 v144, v236, v144
	v_add_f32_e32 v144, v237, v144
	v_add_f32_e32 v239, v249, v144
	v_mov_b32_e32 v240, v239
	v_cvt_pk_bf16_f32 v144, v141, v143
	v_cvt_pk_bf16_f32 v145, v139, v142
	v_cvt_pk_bf16_f32 v146, v137, v140
	v_cvt_pk_bf16_f32 v147, v136, v138
	s_nop 1
	v_permlane32_swap_b32_e32 v239, v240
	v_permlane32_swap_b32_e32 v144, v146
	v_permlane32_swap_b32_e32 v145, v147
	v_cvt_pk_bf16_f32 v226, v133, v135
	v_cvt_pk_bf16_f32 v227, v131, v134
	v_cvt_pk_bf16_f32 v228, v129, v132
	v_cvt_pk_bf16_f32 v229, v128, v130
	v_cvt_pk_bf16_f32 v230, v218, v219
	v_cvt_pk_bf16_f32 v231, v220, v221
	v_cvt_pk_bf16_f32 v232, v238, v241
	v_cvt_pk_bf16_f32 v233, v242, v243
	v_cvt_pk_bf16_f32 v234, v244, v245
	v_cvt_pk_bf16_f32 v235, v246, v247
	v_cvt_pk_bf16_f32 v236, v248, v236
	v_cvt_pk_bf16_f32 v237, v237, v249
	s_nop 0
	v_permlane32_swap_b32_e32 v226, v228
	v_permlane32_swap_b32_e32 v227, v229
	v_permlane32_swap_b32_e32 v230, v232
	v_permlane32_swap_b32_e32 v231, v233
	v_permlane32_swap_b32_e32 v234, v236
	v_permlane32_swap_b32_e32 v235, v237
	ds_read_b128 v[242:245], v158 offset:40960
	ds_read_b128 v[246:249], v161 offset:40960
	s_cmp_lt_u32 s20, 10
	s_cselect_b32 s8, 0, -12
	s_cselect_b32 s9, s13, 0x4000
	s_add_i32 s8, s8, s19
	s_lshl_b32 s8, s8, 6
	s_add_i32 s8, s8, s9
	s_mulk_i32 s8, 0x2400
	s_add_i32 s10, s8, 0x240000
	s_add_u32 s8, s14, s10
	s_addc_u32 s9, s15, 0
	s_add_u32 s10, s16, s10
	s_addc_u32 s11, s17, 0
	v_lshl_add_u64 v[128:129], s[10:11], 0, v[192:193]
	v_lshl_add_u64 v[132:133], s[10:11], 0, v[150:151]
	v_lshl_add_u64 v[136:137], s[8:9], 0, v[192:193]
	v_lshl_add_u64 v[140:141], s[8:9], 0, v[150:151]
	global_load_dwordx4 v[128:131], v[128:129], off
	s_nop 0
	global_load_dwordx4 v[132:135], v[132:133], off
	s_nop 0
	global_load_dwordx4 v[136:139], v[136:137], off
	s_nop 0
	global_load_dwordx4 v[140:143], v[140:141], off
	s_waitcnt lgkmcnt(3)
	v_mfma_f32_32x32x16_bf16 v[80:95], v[64:67], v[100:103], 0
	s_waitcnt lgkmcnt(2)
	v_mfma_f32_32x32x16_bf16 v[80:95], v[250:253], v[104:107], v[80:95]
	ds_read_b128 v[250:253], v162 offset:32768
	s_waitcnt lgkmcnt(2)
	v_mfma_f32_32x32x16_bf16 v[64:79], v[242:245], v[100:103], 0
	ds_read_b128 v[242:245], v162 offset:40960
	s_waitcnt lgkmcnt(2)
	v_mfma_f32_32x32x16_bf16 v[64:79], v[246:249], v[104:107], v[64:79]
	ds_read_b128 v[246:249], v160 offset:32768
	s_waitcnt lgkmcnt(2)
	v_mfma_f32_32x32x16_bf16 v[80:95], v[250:253], v[120:123], v[80:95]
	ds_read_b128 v[250:253], v160 offset:40960
	s_waitcnt lgkmcnt(2)
	v_mfma_f32_32x32x16_bf16 v[64:79], v[242:245], v[120:123], v[64:79]
	ds_read_b128 v[242:245], v166 offset:32768
	s_waitcnt lgkmcnt(2)
	v_mfma_f32_32x32x16_bf16 v[80:95], v[246:249], v[124:127], v[80:95]
	ds_read_b128 v[246:249], v166 offset:40960
	s_waitcnt lgkmcnt(2)
	v_mfma_f32_32x32x16_bf16 v[64:79], v[250:253], v[124:127], v[64:79]
	ds_read_b128 v[250:253], v165 offset:32768
	s_waitcnt lgkmcnt(2)
	v_mfma_f32_32x32x16_bf16 v[80:95], v[242:245], v[116:119], v[80:95]
	ds_read_b128 v[242:245], v165 offset:40960
	s_waitcnt lgkmcnt(2)
	v_mfma_f32_32x32x16_bf16 v[64:79], v[246:249], v[116:119], v[64:79]
	ds_read_b128 v[246:249], v164 offset:32768
	s_waitcnt lgkmcnt(2)
	v_mfma_f32_32x32x16_bf16 v[80:95], v[250:253], v[112:115], v[80:95]
	ds_read_b128 v[250:253], v164 offset:40960
	s_waitcnt lgkmcnt(2)
	v_mfma_f32_32x32x16_bf16 v[64:79], v[242:245], v[112:115], v[64:79]
	ds_read_b128 v[242:245], v163 offset:32768
	s_waitcnt lgkmcnt(2)
	v_mfma_f32_32x32x16_bf16 v[80:95], v[246:249], v[108:111], v[80:95]
	ds_read_b128 v[246:249], v163 offset:40960
	s_waitcnt lgkmcnt(2)
	v_mfma_f32_32x32x16_bf16 v[64:79], v[250:253], v[108:111], v[64:79]
	s_waitcnt lgkmcnt(1)
	v_mfma_f32_32x32x16_bf16 v[80:95], v[242:245], v[96:99], v[80:95]
	s_waitcnt lgkmcnt(0)
	v_mfma_f32_32x32x16_bf16 v[64:79], v[246:249], v[96:99], v[64:79]
	s_cbranch_vccnz .LBB0_618
	v_add3_u32 v218, v215, s19, 3
	v_max_i32_e32 v218, -7, v218
	v_add_u32_e32 v218, 7, v218
	s_add_i32 s8, s12, s19
	v_min_u32_e32 v218, 14, v218
	s_add_i32 s8, s8, 3
	v_mul_u32_u24_e32 v218, 31, v218
	v_cmp_ge_u32_e32 vcc, s8, v169
	v_cmp_lt_u32_e64 s[8:9], s8, v170
	v_sub_u32_e32 v218, v218, v168
	s_and_b64 s[8:9], vcc, s[8:9]
	v_add_u32_e32 v219, 15, v218
	v_mov_b32_e32 v218, 0x1d1
	v_add_u32_e32 v220, v219, v173
	s_and_b64 vcc, s[36:37], s[8:9]
	v_cndmask_b32_e32 v220, v218, v220, vcc
	v_lshl_add_u32 v220, v220, 2, s18
	ds_read_b32 v220, v220
	v_readlane_b32 s10, v255, 28
	v_readlane_b32 s11, v255, 29
	v_readlane_b32 s22, v255, 30
	s_and_b64 s[10:11], s[8:9], s[10:11]
	v_add_u32_e32 v221, v219, v174
	s_and_b64 vcc, s[38:39], s[8:9]
	v_cndmask_b32_e32 v221, v218, v221, vcc
	v_lshl_add_u32 v221, v221, 2, s18
	ds_read_b32 v221, v221
	v_readlane_b32 s23, v255, 31
	v_add_u32_e32 v241, v219, v175
	s_and_b64 vcc, s[40:41], s[8:9]
	v_cndmask_b32_e32 v241, v218, v241, vcc
	v_lshl_add_u32 v241, v241, 2, s18
	ds_read_b32 v241, v241
	v_add_u32_e32 v242, v219, v176
	s_and_b64 vcc, s[42:43], s[8:9]
	v_cndmask_b32_e32 v242, v218, v242, vcc
	v_lshl_add_u32 v242, v242, 2, s18
	ds_read_b32 v242, v242
	v_add_u32_e32 v243, v219, v177
	s_and_b64 vcc, s[8:9], s[44:45]
	v_cndmask_b32_e32 v243, v218, v243, vcc
	v_lshl_add_u32 v243, v243, 2, s18
	ds_read_b32 v243, v243
	v_add_u32_e32 v244, v219, v178
	s_and_b64 vcc, s[8:9], s[46:47]
	v_cndmask_b32_e32 v244, v218, v244, vcc
	v_lshl_add_u32 v244, v244, 2, s18
	ds_read_b32 v244, v244
	v_add_u32_e32 v245, v219, v179
	s_and_b64 vcc, s[8:9], s[48:49]
	v_cndmask_b32_e32 v245, v218, v245, vcc
	v_lshl_add_u32 v245, v245, 2, s18
	ds_read_b32 v245, v245
	v_add_u32_e32 v246, v219, v180
	s_and_b64 vcc, s[8:9], s[50:51]
	v_cndmask_b32_e32 v246, v218, v246, vcc
	v_lshl_add_u32 v246, v246, 2, s18
	ds_read_b32 v246, v246
	v_add_u32_e32 v247, v219, v181
	s_and_b64 vcc, s[10:11], s[22:23]
	v_cndmask_b32_e32 v247, v218, v247, vcc
	v_lshl_add_u32 v247, v247, 2, s18
	ds_read_b32 v247, v247
	v_readlane_b32 s10, v255, 32
	v_readlane_b32 s11, v255, 33
	v_readlane_b32 s22, v255, 34
	s_and_b64 s[10:11], s[8:9], s[10:11]
	v_readlane_b32 s23, v255, 35
	v_add_u32_e32 v248, v219, v182
	s_and_b64 vcc, s[10:11], s[22:23]
	v_cndmask_b32_e32 v248, v218, v248, vcc
	v_lshl_add_u32 v248, v248, 2, s18
	ds_read_b32 v248, v248
	v_readlane_b32 s10, v255, 36
	v_readlane_b32 s11, v255, 37
	v_readlane_b32 s22, v255, 38
	s_and_b64 s[10:11], s[8:9], s[10:11]
	v_readlane_b32 s23, v255, 39
	v_add_u32_e32 v249, v219, v183
	s_and_b64 vcc, s[10:11], s[22:23]
	v_cndmask_b32_e32 v249, v218, v249, vcc
	v_lshl_add_u32 v249, v249, 2, s18
	ds_read_b32 v249, v249
	v_readlane_b32 s10, v255, 40
	v_readlane_b32 s11, v255, 41
	v_readlane_b32 s22, v255, 42
	s_and_b64 s[10:11], s[8:9], s[10:11]
	v_readlane_b32 s23, v255, 43
	v_add_u32_e32 v250, v219, v184
	s_and_b64 vcc, s[10:11], s[22:23]
	v_cndmask_b32_e32 v250, v218, v250, vcc
	v_lshl_add_u32 v250, v250, 2, s18
	ds_read_b32 v250, v250
	v_readlane_b32 s10, v255, 44
	v_readlane_b32 s11, v255, 45
	s_and_b64 s[10:11], s[8:9], s[10:11]
	v_add_u32_e32 v251, v219, v185
	s_and_b64 vcc, s[10:11], s[30:31]
	v_cndmask_b32_e32 v251, v218, v251, vcc
	v_lshl_add_u32 v251, v251, 2, s18
	ds_read_b32 v251, v251
	s_and_b64 s[10:11], s[8:9], s[34:35]
	v_add_u32_e32 v252, v219, v186
	s_and_b64 vcc, s[10:11], s[24:25]
	v_cndmask_b32_e32 v252, v218, v252, vcc
	v_lshl_add_u32 v252, v252, 2, s18
	ds_read_b32 v252, v252
	s_and_b64 s[10:11], s[8:9], s[26:27]
	v_add_u32_e32 v253, v219, v187
	s_and_b64 vcc, s[10:11], s[28:29]
	v_cndmask_b32_e32 v253, v218, v253, vcc
	v_lshl_add_u32 v253, v253, 2, s18
	ds_read_b32 v253, v253
	s_and_b64 s[10:11], s[8:9], s[52:53]
	s_waitcnt lgkmcnt(14)
	v_add_f32_e32 v80, v80, v220
	v_add_u32_e32 v220, v219, v188
	s_and_b64 vcc, s[10:11], s[54:55]
	v_cndmask_b32_e32 v220, v218, v220, vcc
	v_lshl_add_u32 v220, v220, 2, s18
	ds_read_b32 v220, v220
	s_and_b64 s[10:11], s[8:9], s[56:57]
	s_waitcnt lgkmcnt(14)
	v_add_f32_e32 v81, v81, v221
	v_add_u32_e32 v221, v219, v189
	s_and_b64 vcc, s[10:11], s[58:59]
	v_cndmask_b32_e32 v221, v218, v221, vcc
	v_lshl_add_u32 v221, v221, 2, s18
	ds_read_b32 v221, v221
	s_and_b64 s[10:11], s[8:9], s[60:61]
	s_waitcnt lgkmcnt(14)
	v_add_f32_e32 v82, v82, v241
	v_add_u32_e32 v241, v219, v190
	s_and_b64 vcc, s[10:11], s[62:63]
	v_cndmask_b32_e32 v241, v218, v241, vcc
	v_lshl_add_u32 v241, v241, 2, s18
	ds_read_b32 v241, v241
	s_and_b64 s[10:11], s[8:9], s[64:65]
	s_waitcnt lgkmcnt(14)
	v_add_f32_e32 v83, v83, v242
	v_add_u32_e32 v242, v219, v191
	s_and_b64 vcc, s[10:11], s[66:67]
	v_cndmask_b32_e32 v242, v218, v242, vcc
	v_lshl_add_u32 v242, v242, 2, s18
	ds_read_b32 v242, v242
	s_and_b64 s[10:11], s[8:9], s[68:69]
	s_waitcnt lgkmcnt(14)
	v_add_f32_e32 v84, v84, v243
	v_add_u32_e32 v243, v219, v200
	s_and_b64 vcc, s[10:11], s[70:71]
	v_cndmask_b32_e32 v243, v218, v243, vcc
	v_lshl_add_u32 v243, v243, 2, s18
	ds_read_b32 v243, v243
	s_and_b64 s[10:11], s[8:9], s[72:73]
	s_waitcnt lgkmcnt(14)
	v_add_f32_e32 v85, v85, v244
	v_add_u32_e32 v244, v219, v201
	s_and_b64 vcc, s[10:11], s[74:75]
	v_cndmask_b32_e32 v244, v218, v244, vcc
	v_lshl_add_u32 v244, v244, 2, s18
	ds_read_b32 v244, v244
	s_and_b64 s[10:11], s[8:9], s[76:77]
	s_waitcnt lgkmcnt(14)
	v_add_f32_e32 v86, v86, v245
	v_add_u32_e32 v245, v219, v203
	s_and_b64 vcc, s[10:11], s[78:79]
	v_cndmask_b32_e32 v245, v218, v245, vcc
	v_lshl_add_u32 v245, v245, 2, s18
	ds_read_b32 v245, v245
	s_and_b64 s[10:11], s[8:9], s[80:81]
	s_waitcnt lgkmcnt(14)
	v_add_f32_e32 v87, v87, v246
	v_add_u32_e32 v246, v219, v204
	s_and_b64 vcc, s[10:11], s[82:83]
	v_cndmask_b32_e32 v246, v218, v246, vcc
	v_lshl_add_u32 v246, v246, 2, s18
	ds_read_b32 v246, v246
	s_and_b64 s[10:11], s[8:9], s[84:85]
	s_waitcnt lgkmcnt(14)
	v_add_f32_e32 v88, v88, v247
	v_add_u32_e32 v247, v219, v205
	s_and_b64 vcc, s[10:11], s[86:87]
	v_cndmask_b32_e32 v247, v218, v247, vcc
	v_lshl_add_u32 v247, v247, 2, s18
	ds_read_b32 v247, v247
	s_waitcnt lgkmcnt(14)
	v_add_f32_e32 v89, v89, v248
	v_add_u32_e32 v248, v219, v206
	s_and_b64 vcc, s[8:9], s[88:89]
	v_cndmask_b32_e32 v248, v218, v248, vcc
	v_lshl_add_u32 v248, v248, 2, s18
	ds_read_b32 v248, v248
	s_waitcnt lgkmcnt(14)
	v_add_f32_e32 v90, v90, v249
	v_add_u32_e32 v249, v219, v207
	s_and_b64 vcc, s[8:9], s[90:91]
	v_cndmask_b32_e32 v249, v218, v249, vcc
	v_lshl_add_u32 v249, v249, 2, s18
	ds_read_b32 v249, v249
	s_waitcnt lgkmcnt(14)
	v_add_f32_e32 v91, v91, v250
	v_add_u32_e32 v250, v219, v208
	s_and_b64 vcc, s[8:9], s[92:93]
	v_cndmask_b32_e32 v250, v218, v250, vcc
	v_lshl_add_u32 v250, v250, 2, s18
	ds_read_b32 v250, v250
	s_waitcnt lgkmcnt(14)
	v_add_f32_e32 v92, v92, v251
	v_add_u32_e32 v251, v219, v209
	s_and_b64 vcc, s[8:9], s[94:95]
	v_cndmask_b32_e32 v251, v218, v251, vcc
	v_lshl_add_u32 v251, v251, 2, s18
	ds_read_b32 v251, v251
	s_waitcnt lgkmcnt(14)
	v_add_f32_e32 v93, v93, v252
	v_add_u32_e32 v252, v219, v210
	s_and_b64 vcc, s[8:9], s[96:97]
	v_cndmask_b32_e32 v252, v218, v252, vcc
	v_lshl_add_u32 v252, v252, 2, s18
	ds_read_b32 v252, v252
	s_waitcnt lgkmcnt(14)
	v_add_f32_e32 v94, v94, v253
	v_add_u32_e32 v253, v219, v211
	s_and_b64 vcc, s[8:9], s[2:3]
	v_cndmask_b32_e32 v253, v218, v253, vcc
	v_lshl_add_u32 v253, v253, 2, s18
	ds_read_b32 v253, v253
	s_waitcnt lgkmcnt(14)
	v_add_f32_e32 v95, v95, v220
	v_add_u32_e32 v220, v219, v212
	s_and_b64 vcc, s[8:9], s[0:1]
	v_cndmask_b32_e32 v220, v218, v220, vcc
	v_lshl_add_u32 v220, v220, 2, s18
	ds_read_b32 v220, v220
	s_waitcnt lgkmcnt(14)
	v_add_f32_e32 v64, v64, v221
	v_add_u32_e32 v221, v219, v213
	s_and_b64 vcc, s[8:9], s[6:7]
	v_cndmask_b32_e32 v221, v218, v221, vcc
	v_lshl_add_u32 v221, v221, 2, s18
	ds_read_b32 v221, v221
	s_waitcnt lgkmcnt(14)
	v_add_f32_e32 v65, v65, v241
	s_waitcnt lgkmcnt(13)
	v_add_f32_e32 v66, v66, v242
	s_waitcnt lgkmcnt(12)
	v_add_f32_e32 v67, v67, v243
	s_waitcnt lgkmcnt(11)
	v_add_f32_e32 v68, v68, v244
	s_waitcnt lgkmcnt(10)
	v_add_f32_e32 v69, v69, v245
	s_waitcnt lgkmcnt(9)
	v_add_f32_e32 v70, v70, v246
	s_waitcnt lgkmcnt(8)
	v_add_f32_e32 v71, v71, v247
	s_waitcnt lgkmcnt(7)
	v_add_f32_e32 v72, v72, v248
	s_waitcnt lgkmcnt(6)
	v_add_f32_e32 v73, v73, v249
	s_waitcnt lgkmcnt(5)
	v_add_f32_e32 v74, v74, v250
	s_waitcnt lgkmcnt(4)
	v_add_f32_e32 v75, v75, v251
	s_waitcnt lgkmcnt(3)
	v_add_f32_e32 v76, v76, v252
	s_waitcnt lgkmcnt(2)
	v_add_f32_e32 v77, v77, v253
	s_waitcnt lgkmcnt(1)
	v_add_f32_e32 v78, v78, v220
	s_waitcnt lgkmcnt(0)
	v_add_f32_e32 v79, v79, v221
.LBB0_618:
	s_cmp_eq_u32 s100, 1
	s_cbranch_scc1 .Lna_pvdA
	ds_read_b64_tr_b16 v[242:243], v167 offset:0
	ds_read_b64_tr_b16 v[244:245], v167 offset:0x800
	ds_read_b64_tr_b16 v[246:247], v167 offset:0x1000
	ds_read_b64_tr_b16 v[248:249], v167 offset:0x1800
	ds_read_b64_tr_b16 v[250:251], v167 offset:0x2000
	ds_read_b64_tr_b16 v[252:253], v167 offset:0x2800
	ds_read_b64_tr_b16 v[218:219], v167 offset:0x3000
	ds_read_b64_tr_b16 v[220:221], v167 offset:0x3800
	s_waitcnt lgkmcnt(0)
	s_nop 0
	v_mfma_f32_32x32x16_bf16 v[0:15], v[144:147], v[242:245], v[0:15]
	v_mfma_f32_32x32x16_bf16 v[0:15], v[226:229], v[246:249], v[0:15]
	v_mfma_f32_32x32x16_bf16 v[0:15], v[230:233], v[250:253], v[0:15]
	v_mfma_f32_32x32x16_bf16 v[0:15], v[234:237], v[218:221], v[0:15]
	ds_read_b64_tr_b16 v[218:219], v167 offset:0x200
	ds_read_b64_tr_b16 v[220:221], v167 offset:0xa00
	ds_read_b64_tr_b16 v[242:243], v167 offset:0x1200
	ds_read_b64_tr_b16 v[244:245], v167 offset:0x1a00
	ds_read_b64_tr_b16 v[246:247], v167 offset:0x2200
	ds_read_b64_tr_b16 v[248:249], v167 offset:0x2a00
	ds_read_b64_tr_b16 v[250:251], v167 offset:0x3200
	ds_read_b64_tr_b16 v[252:253], v167 offset:0x3a00
	s_waitcnt lgkmcnt(0)
	s_nop 0
	v_mfma_f32_32x32x16_bf16 v[48:63], v[144:147], v[218:221], v[48:63]
	ds_read_b64_tr_b16 v[218:219], v167 offset:0x400
	ds_read_b64_tr_b16 v[220:221], v167 offset:0xc00
	v_mfma_f32_32x32x16_bf16 v[48:63], v[226:229], v[242:245], v[48:63]
	ds_read_b64_tr_b16 v[242:243], v167 offset:0x1400
	ds_read_b64_tr_b16 v[244:245], v167 offset:0x1c00
	v_mfma_f32_32x32x16_bf16 v[48:63], v[230:233], v[246:249], v[48:63]
	ds_read_b64_tr_b16 v[246:247], v167 offset:0x2400
	ds_read_b64_tr_b16 v[248:249], v167 offset:0x2c00
	v_mfma_f32_32x32x16_bf16 v[48:63], v[234:237], v[250:253], v[48:63]
	ds_read_b64_tr_b16 v[250:251], v167 offset:0x3400
	ds_read_b64_tr_b16 v[252:253], v167 offset:0x3c00
	s_waitcnt lgkmcnt(0)
	v_mfma_f32_32x32x16_bf16 v[32:47], v[144:147], v[218:221], v[32:47]
	ds_read_b64_tr_b16 v[218:219], v167 offset:0x600
	ds_read_b64_tr_b16 v[220:221], v167 offset:0xe00
	v_mfma_f32_32x32x16_bf16 v[32:47], v[226:229], v[242:245], v[32:47]
	ds_read_b64_tr_b16 v[242:243], v167 offset:0x1600
	ds_read_b64_tr_b16 v[244:245], v167 offset:0x1e00
	v_mfma_f32_32x32x16_bf16 v[32:47], v[230:233], v[246:249], v[32:47]
	ds_read_b64_tr_b16 v[246:247], v167 offset:0x2600
	ds_read_b64_tr_b16 v[248:249], v167 offset:0x2e00
	v_mfma_f32_32x32x16_bf16 v[32:47], v[234:237], v[250:253], v[32:47]
	ds_read_b64_tr_b16 v[250:251], v167 offset:0x3600
	ds_read_b64_tr_b16 v[252:253], v167 offset:0x3e00
	s_waitcnt lgkmcnt(0)
	v_mfma_f32_32x32x16_bf16 v[16:31], v[144:147], v[218:221], v[16:31]
	v_max_f32_e32 v144, v81, v81
	v_max_f32_e32 v145, v80, v80
	v_max_f32_e32 v144, v145, v144
	v_max3_f32 v144, v144, v82, v83
	v_max3_f32 v144, v144, v84, v85
	v_max3_f32 v144, v144, v86, v87
	v_max3_f32 v144, v144, v88, v89
	v_max3_f32 v144, v144, v90, v91
	v_max3_f32 v144, v144, v92, v93
	v_mfma_f32_32x32x16_bf16 v[16:31], v[226:229], v[242:245], v[16:31]
	v_max3_f32 v144, v144, v94, v95
	v_max3_f32 v144, v144, v64, v65
	v_max3_f32 v144, v144, v66, v67
	v_max3_f32 v144, v144, v68, v69
	v_max3_f32 v144, v144, v70, v71
	v_max3_f32 v144, v144, v72, v73
	v_max3_f32 v144, v144, v74, v75
	v_max3_f32 v144, v144, v76, v77
	v_mfma_f32_32x32x16_bf16 v[16:31], v[230:233], v[246:249], v[16:31]
	v_max3_f32 v144, v144, v78, v79
	v_mov_b32_e32 v145, v144
	s_nop 1
	v_permlane32_swap_b32_e32 v144, v145
	v_max_f32_e32 v145, v145, v145
	v_max_f32_e32 v144, v144, v144
	v_max_f32_e32 v144, v144, v145
	v_sub_f32_e32 v145, v144, v222
	s_mov_b32 s8, 0x42b504f3
	v_cmp_ge_f32_e32 vcc, s8, v145
	v_max_f32_e32 v145, v222, v222
	v_max_f32_e32 v145, v145, v144
	v_mfma_f32_32x32x16_bf16 v[16:31], v[234:237], v[250:253], v[16:31]
	v_sub_f32_e32 v144, v222, v145
	v_mul_f32_e32 v144, 0x3e0293ee, v144
	v_exp_f32_e32 v144, v144
	s_cmp_eq_u64 vcc, exec
	s_cselect_b64 s[8:9], -1, 0
.Lna_pvjA:
	s_barrier
	s_waitcnt vmcnt(0)
	v_cndmask_b32_e64 v144, v144, 1.0, s[8:9]
	v_cmp_gt_f32_e32 vcc, 1.0, v144
	s_waitcnt vmcnt(3)
	ds_write_b128 v156, v[128:131] offset:16384
	s_waitcnt vmcnt(2)
	ds_write_b128 v157, v[132:135] offset:16384
	s_waitcnt vmcnt(1)
	ds_write_b128 v153, v[136:139] offset:49152
	s_waitcnt vmcnt(0)
	ds_write_b128 v155, v[140:143] offset:49152
	s_cbranch_vccz .LBB0_622
	s_and_saveexec_b64 s[10:11], s[4:5]
	ds_write_b32 v171, v144 offset:128
	s_or_b64 exec, exec, s[10:11]
	s_waitcnt lgkmcnt(0)
	v_add_u32_e32 v140, v159, v148
	ds_read_b128 v[128:131], v140 offset:224
	ds_read_b128 v[132:135], v140 offset:192
	ds_read_b128 v[136:139], v140 offset:160
	ds_read_b128 v[140:143], v140 offset:128
	s_waitcnt lgkmcnt(3)
	v_pk_mul_f32 v[12:13], v[12:13], v[128:129]
	s_waitcnt lgkmcnt(2)
	v_pk_mul_f32 v[8:9], v[8:9], v[132:133]
	s_waitcnt lgkmcnt(1)
	v_pk_mul_f32 v[4:5], v[4:5], v[136:137]
	v_pk_mul_f32 v[14:15], v[14:15], v[130:131]
	v_pk_mul_f32 v[10:11], v[10:11], v[134:135]
	v_pk_mul_f32 v[6:7], v[6:7], v[138:139]
	s_waitcnt lgkmcnt(0)
	v_pk_mul_f32 v[2:3], v[2:3], v[142:143]
	v_pk_mul_f32 v[0:1], v[0:1], v[140:141]
	v_pk_mul_f32 v[60:61], v[60:61], v[128:129]
	v_pk_mul_f32 v[56:57], v[56:57], v[132:133]
	v_pk_mul_f32 v[52:53], v[52:53], v[136:137]
	v_pk_mul_f32 v[62:63], v[62:63], v[130:131]
	v_pk_mul_f32 v[58:59], v[58:59], v[134:135]
	v_pk_mul_f32 v[54:55], v[54:55], v[138:139]
	v_pk_mul_f32 v[50:51], v[50:51], v[142:143]
	v_pk_mul_f32 v[48:49], v[48:49], v[140:141]
	v_pk_mul_f32 v[44:45], v[44:45], v[128:129]
	v_pk_mul_f32 v[40:41], v[40:41], v[132:133]
	v_pk_mul_f32 v[36:37], v[36:37], v[136:137]
	v_pk_mul_f32 v[46:47], v[46:47], v[130:131]
	v_pk_mul_f32 v[42:43], v[42:43], v[134:135]
	v_pk_mul_f32 v[38:39], v[38:39], v[138:139]
	v_pk_mul_f32 v[34:35], v[34:35], v[142:143]
	v_pk_mul_f32 v[32:33], v[32:33], v[140:141]
	v_pk_mul_f32 v[28:29], v[28:29], v[128:129]
	v_pk_mul_f32 v[24:25], v[24:25], v[132:133]
	v_pk_mul_f32 v[20:21], v[20:21], v[136:137]
	v_pk_mul_f32 v[30:31], v[30:31], v[130:131]
	v_pk_mul_f32 v[26:27], v[26:27], v[134:135]
	v_pk_mul_f32 v[22:23], v[22:23], v[138:139]
	v_pk_mul_f32 v[18:19], v[18:19], v[142:143]
	v_pk_mul_f32 v[16:17], v[16:17], v[140:141]

.Lna_deadA:
	v_add_f32_e32 v144, 0, v236
	v_add_f32_e32 v144, v238, v144
	v_add_f32_e32 v144, v145, v144
	v_add_f32_e32 v144, v237, v144
	v_add_f32_e32 v144, v146, v144
	v_add_f32_e32 v144, v235, v144
	v_add_f32_e32 v144, v147, v144
	v_add_f32_e32 v144, v234, v144
	v_add_f32_e32 v144, v231, v144
	v_add_f32_e32 v144, v233, v144
	v_add_f32_e32 v144, v230, v144
	v_add_f32_e32 v144, v232, v144
	v_exp_f32_e32 v134, v134
	v_add_f32_e32 v144, v227, v144
	v_exp_f32_e32 v135, v135
	v_add_f32_e32 v144, v229, v144
	v_exp_f32_e32 v138, v138
	v_add_f32_e32 v144, v226, v144
	v_exp_f32_e32 v139, v139
	v_add_f32_e32 v144, v228, v144
	v_exp_f32_e32 v130, v130
	v_add_f32_e32 v144, v134, v144
	v_exp_f32_e32 v131, v131
	v_add_f32_e32 v144, v135, v144
	v_exp_f32_e32 v132, v132
	v_add_f32_e32 v144, v138, v144
	v_exp_f32_e32 v133, v133
	v_add_f32_e32 v144, v139, v144
	v_exp_f32_e32 v136, v136
	v_add_f32_e32 v144, v130, v144
	v_exp_f32_e32 v137, v137
	v_add_f32_e32 v144, v131, v144
	v_exp_f32_e32 v142, v142
	v_add_f32_e32 v144, v132, v144
	v_exp_f32_e32 v143, v143
	v_add_f32_e32 v144, v133, v144
	v_exp_f32_e32 v140, v140
	v_add_f32_e32 v144, v136, v144
	v_exp_f32_e32 v141, v141
	v_add_f32_e32 v144, v137, v144
	v_exp_f32_e32 v128, v128
	v_add_f32_e32 v144, v142, v144
	v_exp_f32_e32 v129, v129
	v_add_f32_e32 v144, v143, v144
	v_add_f32_e32 v144, v140, v144
	v_add_f32_e32 v144, v141, v144
	v_add_f32_e32 v144, v128, v144
	v_add_f32_e32 v223, v129, v144
	v_mov_b32_e32 v224, v223
	v_cvt_pk_bf16_f32 v144, v236, v238
	v_cvt_pk_bf16_f32 v145, v145, v237
	v_cvt_pk_bf16_f32 v146, v146, v235
	s_nop 0
	v_permlane32_swap_b32_e32 v223, v224
	v_cvt_pk_bf16_f32 v147, v147, v234
	v_permlane32_swap_b32_e32 v144, v146
	v_cvt_pk_bf16_f32 v234, v231, v233
	v_cvt_pk_bf16_f32 v235, v230, v232
	v_cvt_pk_bf16_f32 v236, v227, v229
	v_cvt_pk_bf16_f32 v237, v226, v228
	v_cvt_pk_bf16_f32 v226, v134, v135
	v_cvt_pk_bf16_f32 v227, v138, v139
	v_cvt_pk_bf16_f32 v228, v130, v131
	v_cvt_pk_bf16_f32 v229, v132, v133
	v_cvt_pk_bf16_f32 v230, v136, v137
	v_cvt_pk_bf16_f32 v231, v142, v143
	v_cvt_pk_bf16_f32 v232, v140, v141
	v_cvt_pk_bf16_f32 v233, v128, v129
	v_permlane32_swap_b32_e32 v145, v147
	v_permlane32_swap_b32_e32 v234, v236
	v_permlane32_swap_b32_e32 v235, v237
	v_permlane32_swap_b32_e32 v226, v228
	v_permlane32_swap_b32_e32 v227, v229
	v_permlane32_swap_b32_e32 v230, v232
	v_permlane32_swap_b32_e32 v231, v233
	s_add_i32 s8, s19, 3
	s_cmp_lt_u32 s8, 12
	s_cselect_b64 s[10:11], -1, 0
	s_and_b64 s[8:9], s[10:11], exec
	s_cselect_b32 s8, 0, -12
	s_cselect_b32 s9, s13, 0x4000
	s_add_i32 s8, s8, s19
	s_lshl_b32 s8, s8, 6
	s_add_i32 s8, s8, s9
	s_mulk_i32 s8, 0x2400
	s_add_i32 s21, s8, 0x1b0000
	s_add_u32 s8, s14, s21
	s_addc_u32 s9, s15, 0
	s_add_u32 vcc_lo, s16, s21
	s_addc_u32 vcc_hi, s17, 0
	v_lshl_add_u64 v[128:129], vcc, 0, v[192:193]
	v_lshl_add_u64 v[132:133], vcc, 0, v[150:151]
	v_lshl_add_u64 v[136:137], s[8:9], 0, v[192:193]
	v_lshl_add_u64 v[140:141], s[8:9], 0, v[150:151]
	global_load_dwordx4 v[128:131], v[128:129], off
	s_nop 0
	global_load_dwordx4 v[132:135], v[132:133], off
	s_nop 0
	global_load_dwordx4 v[136:139], v[136:137], off
	s_nop 0
	global_load_dwordx4 v[140:143], v[140:141], off
	v_mov_b32_e32 v64, v217
	v_mov_b32_e32 v65, v217
	v_mov_b32_e32 v66, v217
	v_mov_b32_e32 v67, v217
	v_mov_b32_e32 v68, v217
	v_mov_b32_e32 v69, v217
	v_mov_b32_e32 v70, v217
	v_mov_b32_e32 v71, v217
	v_mov_b32_e32 v72, v217
	v_mov_b32_e32 v73, v217
	v_mov_b32_e32 v74, v217
	v_mov_b32_e32 v75, v217
	v_mov_b32_e32 v76, v217
	v_mov_b32_e32 v77, v217
	v_mov_b32_e32 v78, v217
	v_mov_b32_e32 v79, v217
	v_mov_b32_e32 v80, v217
	v_mov_b32_e32 v81, v217
	v_mov_b32_e32 v82, v217
	v_mov_b32_e32 v83, v217
	v_mov_b32_e32 v84, v217
	v_mov_b32_e32 v85, v217
	v_mov_b32_e32 v86, v217
	v_mov_b32_e32 v87, v217
	v_mov_b32_e32 v88, v217
	v_mov_b32_e32 v89, v217
	v_mov_b32_e32 v90, v217
	v_mov_b32_e32 v91, v217
	v_mov_b32_e32 v92, v217
	v_mov_b32_e32 v93, v217
	v_mov_b32_e32 v94, v217
	v_mov_b32_e32 v95, v217
	s_mov_b32 s100, 1
	s_branch .LBB0_612
.Lna_deadB:
	s_andn2_b64 vcc, exec, s[10:11]
	v_exp_f32_e32 v249, v144
	v_add_f32_e32 v144, 0, v141
	v_add_f32_e32 v144, v143, v144
	v_add_f32_e32 v144, v139, v144
	v_add_f32_e32 v144, v142, v144
	v_add_f32_e32 v144, v137, v144
	v_add_f32_e32 v144, v140, v144
	v_add_f32_e32 v144, v136, v144
	v_add_f32_e32 v144, v138, v144
	v_add_f32_e32 v144, v133, v144
	v_add_f32_e32 v144, v135, v144
	v_add_f32_e32 v144, v131, v144
	v_add_f32_e32 v144, v134, v144
	v_exp_f32_e32 v218, v145
	v_add_f32_e32 v144, v129, v144
	v_exp_f32_e32 v219, v146
	v_add_f32_e32 v144, v132, v144
	v_exp_f32_e32 v220, v147
	v_add_f32_e32 v144, v128, v144
	v_exp_f32_e32 v221, v226
	v_add_f32_e32 v144, v130, v144
	v_exp_f32_e32 v238, v227
	v_add_f32_e32 v144, v218, v144
	v_exp_f32_e32 v241, v228
	v_add_f32_e32 v144, v219, v144
	v_exp_f32_e32 v242, v229
	v_add_f32_e32 v144, v220, v144
	v_exp_f32_e32 v243, v230
	v_add_f32_e32 v144, v221, v144
	v_exp_f32_e32 v244, v231
	v_add_f32_e32 v144, v238, v144
	v_exp_f32_e32 v245, v232
	v_add_f32_e32 v144, v241, v144
	v_exp_f32_e32 v246, v233
	v_add_f32_e32 v144, v242, v144
	v_exp_f32_e32 v247, v234
	v_add_f32_e32 v144, v243, v144
	v_exp_f32_e32 v248, v235
	v_add_f32_e32 v144, v244, v144
	v_exp_f32_e32 v236, v236
	v_add_f32_e32 v144, v245, v144
	v_exp_f32_e32 v237, v237
	v_add_f32_e32 v144, v246, v144
	v_add_f32_e32 v144, v247, v144
	v_add_f32_e32 v144, v248, v144
	v_add_f32_e32 v144, v236, v144
	v_add_f32_e32 v144, v237, v144
	v_add_f32_e32 v239, v249, v144
	v_mov_b32_e32 v240, v239
	v_cvt_pk_bf16_f32 v144, v141, v143
	v_cvt_pk_bf16_f32 v145, v139, v142
	v_cvt_pk_bf16_f32 v146, v137, v140
	v_cvt_pk_bf16_f32 v147, v136, v138
	s_nop 1
	v_permlane32_swap_b32_e32 v239, v240
	v_permlane32_swap_b32_e32 v144, v146
	v_permlane32_swap_b32_e32 v145, v147
	v_cvt_pk_bf16_f32 v226, v133, v135
	v_cvt_pk_bf16_f32 v227, v131, v134
	v_cvt_pk_bf16_f32 v228, v129, v132
	v_cvt_pk_bf16_f32 v229, v128, v130
	v_cvt_pk_bf16_f32 v230, v218, v219
	v_cvt_pk_bf16_f32 v231, v220, v221
	v_cvt_pk_bf16_f32 v232, v238, v241
	v_cvt_pk_bf16_f32 v233, v242, v243
	v_cvt_pk_bf16_f32 v234, v244, v245
	v_cvt_pk_bf16_f32 v235, v246, v247
	v_cvt_pk_bf16_f32 v236, v248, v236
	v_cvt_pk_bf16_f32 v237, v237, v249
	s_nop 0
	v_permlane32_swap_b32_e32 v226, v228
	v_permlane32_swap_b32_e32 v227, v229
	v_permlane32_swap_b32_e32 v230, v232
	v_permlane32_swap_b32_e32 v231, v233
	v_permlane32_swap_b32_e32 v234, v236
	v_permlane32_swap_b32_e32 v235, v237
	s_cmp_lt_u32 s20, 10
	s_cselect_b32 s8, 0, -12
	s_cselect_b32 s9, s13, 0x4000
	s_add_i32 s8, s8, s19
	s_lshl_b32 s8, s8, 6
	s_add_i32 s8, s8, s9
	s_mulk_i32 s8, 0x2400
	s_add_i32 s10, s8, 0x240000
	s_add_u32 s8, s14, s10
	s_addc_u32 s9, s15, 0
	s_add_u32 s10, s16, s10
	s_addc_u32 s11, s17, 0
	v_lshl_add_u64 v[128:129], s[10:11], 0, v[192:193]
	v_lshl_add_u64 v[132:133], s[10:11], 0, v[150:151]
	v_lshl_add_u64 v[136:137], s[8:9], 0, v[192:193]
	v_lshl_add_u64 v[140:141], s[8:9], 0, v[150:151]
	global_load_dwordx4 v[128:131], v[128:129], off
	s_nop 0
	global_load_dwordx4 v[132:135], v[132:133], off
	s_nop 0
	global_load_dwordx4 v[136:139], v[136:137], off
	s_nop 0
	global_load_dwordx4 v[140:143], v[140:141], off
	v_mov_b32_e32 v64, v217
	v_mov_b32_e32 v65, v217
	v_mov_b32_e32 v66, v217
	v_mov_b32_e32 v67, v217
	v_mov_b32_e32 v68, v217
	v_mov_b32_e32 v69, v217
	v_mov_b32_e32 v70, v217
	v_mov_b32_e32 v71, v217
	v_mov_b32_e32 v72, v217
	v_mov_b32_e32 v73, v217
	v_mov_b32_e32 v74, v217
	v_mov_b32_e32 v75, v217
	v_mov_b32_e32 v76, v217
	v_mov_b32_e32 v77, v217
	v_mov_b32_e32 v78, v217
	v_mov_b32_e32 v79, v217
	v_mov_b32_e32 v80, v217
	v_mov_b32_e32 v81, v217
	v_mov_b32_e32 v82, v217
	v_mov_b32_e32 v83, v217
	v_mov_b32_e32 v84, v217
	v_mov_b32_e32 v85, v217
	v_mov_b32_e32 v86, v217
	v_mov_b32_e32 v87, v217
	v_mov_b32_e32 v88, v217
	v_mov_b32_e32 v89, v217
	v_mov_b32_e32 v90, v217
	v_mov_b32_e32 v91, v217
	v_mov_b32_e32 v92, v217
	v_mov_b32_e32 v93, v217
	v_mov_b32_e32 v94, v217
	v_mov_b32_e32 v95, v217
	s_mov_b32 s101, 1
	s_branch .LBB0_618
.Lna_pvdA:
	v_max_f32_e32 v144, v81, v81
	v_max_f32_e32 v145, v80, v80
	v_max_f32_e32 v144, v145, v144
	v_max3_f32 v144, v144, v82, v83
	v_max3_f32 v144, v144, v84, v85
	v_max3_f32 v144, v144, v86, v87
	v_max3_f32 v144, v144, v88, v89
	v_max3_f32 v144, v144, v90, v91
	v_max3_f32 v144, v144, v92, v93
	v_max3_f32 v144, v144, v94, v95
	v_max3_f32 v144, v144, v64, v65
	v_max3_f32 v144, v144, v66, v67
	v_max3_f32 v144, v144, v68, v69
	v_max3_f32 v144, v144, v70, v71
	v_max3_f32 v144, v144, v72, v73
	v_max3_f32 v144, v144, v74, v75
	v_max3_f32 v144, v144, v76, v77
	v_max3_f32 v144, v144, v78, v79
	v_mov_b32_e32 v145, v144
	s_nop 1
	v_permlane32_swap_b32_e32 v144, v145
	v_max_f32_e32 v145, v145, v145
	v_max_f32_e32 v144, v144, v144
	v_max_f32_e32 v144, v144, v145
	v_sub_f32_e32 v145, v144, v222
	s_mov_b32 s8, 0x42b504f3
	v_cmp_ge_f32_e32 vcc, s8, v145
	v_max_f32_e32 v145, v222, v222
	v_max_f32_e32 v145, v145, v144
	v_sub_f32_e32 v144, v222, v145
	v_mul_f32_e32 v144, 0x3e0293ee, v144
	v_exp_f32_e32 v144, v144
	s_cmp_eq_u64 vcc, exec
	s_cselect_b64 s[8:9], -1, 0
	s_branch .Lna_pvjA
.Lna_pvdB:
	v_max_f32_e32 v144, v81, v81
	v_max_f32_e32 v145, v80, v80
	v_max_f32_e32 v144, v145, v144
	v_max3_f32 v144, v144, v82, v83
	v_max3_f32 v144, v144, v84, v85
	v_max3_f32 v144, v144, v86, v87
	v_max3_f32 v144, v144, v88, v89
	v_max3_f32 v144, v144, v90, v91
	v_max3_f32 v144, v144, v92, v93
	v_max3_f32 v144, v144, v94, v95
	v_max3_f32 v144, v144, v64, v65
	v_max3_f32 v144, v144, v66, v67
	v_max3_f32 v144, v144, v68, v69
	v_max3_f32 v144, v144, v70, v71
	v_max3_f32 v144, v144, v72, v73
	v_max3_f32 v144, v144, v74, v75
	v_max3_f32 v144, v144, v76, v77
	v_max3_f32 v144, v144, v78, v79
	v_mov_b32_e32 v145, v144
	s_nop 1
	v_permlane32_swap_b32_e32 v144, v145
	v_max_f32_e32 v145, v145, v145
	v_max_f32_e32 v144, v144, v144
	v_max_f32_e32 v144, v144, v145
	v_sub_f32_e32 v145, v144, v222
	s_mov_b32 s8, 0x42b504f3
	v_cmp_ge_f32_e32 vcc, s8, v145
	v_max_f32_e32 v145, v222, v222
	v_max_f32_e32 v144, v145, v144
	v_sub_f32_e32 v145, v222, v144
	v_mul_f32_e32 v145, 0x3e0293ee, v145
	v_exp_f32_e32 v145, v145
	s_cmp_eq_u64 vcc, exec
	s_cselect_b64 s[8:9], -1, 0
	s_branch .Lna_pvjB
.LBB0_624:
	s_mov_b32 s101, 0
	ds_read_b128 v[64:67], v158 offset:49152
	ds_read_b128 v[68:71], v158 offset:57344
	s_waitcnt lgkmcnt(1)
	v_mfma_f32_32x32x16_bf16 v[80:95], v[64:67], v[100:103], 0
	s_waitcnt lgkmcnt(0)
	v_mfma_f32_32x32x16_bf16 v[64:79], v[68:71], v[100:103], 0
	ds_read_b128 v[100:103], v161 offset:49152
	ds_read_b128 v[174:177], v161 offset:57344
	s_waitcnt lgkmcnt(1)
	v_mfma_f32_32x32x16_bf16 v[80:95], v[100:103], v[104:107], v[80:95]
	s_waitcnt lgkmcnt(0)
	v_mfma_f32_32x32x16_bf16 v[64:79], v[174:177], v[104:107], v[64:79]
	ds_read_b128 v[100:103], v162 offset:49152
	ds_read_b128 v[104:107], v162 offset:57344
	s_waitcnt lgkmcnt(1)
	v_mfma_f32_32x32x16_bf16 v[80:95], v[100:103], v[120:123], v[80:95]
	s_waitcnt lgkmcnt(0)
	v_mfma_f32_32x32x16_bf16 v[64:79], v[104:107], v[120:123], v[64:79]
	ds_read_b128 v[100:103], v160 offset:49152
	ds_read_b128 v[104:107], v160 offset:57344
	v_exp_f32_e32 v120, v128
	v_exp_f32_e32 v121, v129
	s_waitcnt lgkmcnt(1)
	v_mfma_f32_32x32x16_bf16 v[80:95], v[100:103], v[124:127], v[80:95]
	s_waitcnt lgkmcnt(0)
	v_mfma_f32_32x32x16_bf16 v[64:79], v[104:107], v[124:127], v[64:79]
	ds_read_b128 v[100:103], v166 offset:49152
	ds_read_b128 v[104:107], v166 offset:57344
	s_waitcnt lgkmcnt(1)
	v_mfma_f32_32x32x16_bf16 v[80:95], v[100:103], v[116:119], v[80:95]
	s_waitcnt lgkmcnt(0)
	v_mfma_f32_32x32x16_bf16 v[64:79], v[104:107], v[116:119], v[64:79]
	ds_read_b128 v[100:103], v165 offset:49152
	ds_read_b128 v[104:107], v165 offset:57344
	v_exp_f32_e32 v116, v142
	v_exp_f32_e32 v117, v143
	v_exp_f32_e32 v118, v140
	v_exp_f32_e32 v119, v141
	s_waitcnt lgkmcnt(1)
	v_mfma_f32_32x32x16_bf16 v[80:95], v[100:103], v[112:115], v[80:95]
	s_waitcnt lgkmcnt(0)
	v_mfma_f32_32x32x16_bf16 v[64:79], v[104:107], v[112:115], v[64:79]
	ds_read_b128 v[100:103], v164 offset:49152
	ds_read_b128 v[104:107], v164 offset:57344
	v_exp_f32_e32 v112, v132
	v_exp_f32_e32 v113, v133
	v_exp_f32_e32 v114, v136
	v_exp_f32_e32 v115, v137
	s_waitcnt lgkmcnt(1)
	v_mfma_f32_32x32x16_bf16 v[80:95], v[100:103], v[108:111], v[80:95]
	s_waitcnt lgkmcnt(0)
	v_mfma_f32_32x32x16_bf16 v[64:79], v[104:107], v[108:111], v[64:79]
	ds_read_b128 v[100:103], v163 offset:49152
	ds_read_b128 v[104:107], v163 offset:57344
	v_exp_f32_e32 v108, v138
	v_exp_f32_e32 v109, v139
	v_exp_f32_e32 v110, v130
	v_exp_f32_e32 v111, v131
	s_waitcnt lgkmcnt(1)
	v_mfma_f32_32x32x16_bf16 v[80:95], v[100:103], v[96:99], v[80:95]
	s_waitcnt lgkmcnt(0)
	v_mfma_f32_32x32x16_bf16 v[64:79], v[104:107], v[96:99], v[64:79]
	v_add_f32_e32 v96, 0, v236
	v_add_f32_e32 v96, v238, v96
	v_add_f32_e32 v96, v145, v96
	v_add_f32_e32 v96, v237, v96
	v_add_f32_e32 v96, v146, v96
	v_add_f32_e32 v96, v235, v96
	v_add_f32_e32 v96, v147, v96
	v_add_f32_e32 v96, v234, v96
	v_add_f32_e32 v96, v231, v96
	v_add_f32_e32 v96, v233, v96
	v_add_f32_e32 v96, v230, v96
	v_add_f32_e32 v96, v232, v96
	v_exp_f32_e32 v106, v134
	v_add_f32_e32 v96, v227, v96
	v_exp_f32_e32 v107, v135
	v_add_f32_e32 v96, v229, v96
	v_add_f32_e32 v96, v226, v96
	v_add_f32_e32 v96, v228, v96
	v_add_f32_e32 v96, v106, v96
	v_add_f32_e32 v96, v107, v96
	v_add_f32_e32 v96, v108, v96
	v_add_f32_e32 v96, v109, v96
	v_add_f32_e32 v96, v110, v96
	v_add_f32_e32 v96, v111, v96
	v_add_f32_e32 v96, v112, v96
	v_add_f32_e32 v96, v113, v96
	v_add_f32_e32 v96, v114, v96
	v_add_f32_e32 v96, v115, v96
	v_add_f32_e32 v96, v116, v96
	v_add_f32_e32 v96, v117, v96
	v_add_f32_e32 v96, v118, v96
	v_add_f32_e32 v96, v119, v96
	v_add_f32_e32 v96, v120, v96
	v_add_f32_e32 v96, v121, v96
	v_mov_b32_e32 v97, v96
	v_cvt_pk_bf16_f32 v98, v236, v238
	v_cvt_pk_bf16_f32 v99, v145, v237
	v_cvt_pk_bf16_f32 v100, v146, v235
	v_cvt_pk_bf16_f32 v101, v147, v234
	s_nop 1
	v_permlane32_swap_b32_e32 v96, v97
	v_permlane32_swap_b32_e32 v98, v100
	v_permlane32_swap_b32_e32 v99, v101
	v_cvt_pk_bf16_f32 v102, v231, v233
	v_cvt_pk_bf16_f32 v103, v230, v232
	v_cvt_pk_bf16_f32 v104, v227, v229
	v_cvt_pk_bf16_f32 v105, v226, v228
	v_cvt_pk_bf16_f32 v106, v106, v107
	v_cvt_pk_bf16_f32 v107, v108, v109
	v_cvt_pk_bf16_f32 v108, v110, v111
	v_cvt_pk_bf16_f32 v109, v112, v113
	v_cvt_pk_bf16_f32 v110, v114, v115
	v_cvt_pk_bf16_f32 v111, v116, v117
	v_cvt_pk_bf16_f32 v112, v118, v119
	v_cvt_pk_bf16_f32 v113, v120, v121
	s_nop 0
	v_permlane32_swap_b32_e32 v102, v104
	v_permlane32_swap_b32_e32 v103, v105
	v_permlane32_swap_b32_e32 v106, v108
	v_permlane32_swap_b32_e32 v107, v109
	v_permlane32_swap_b32_e32 v110, v112
	v_permlane32_swap_b32_e32 v111, v113
	ds_read_b64_tr_b16 v[114:115], v202 offset:0
	ds_read_b64_tr_b16 v[116:117], v202 offset:0x800
	ds_read_b64_tr_b16 v[118:119], v202 offset:0x1000
	ds_read_b64_tr_b16 v[120:121], v202 offset:0x1800
	ds_read_b64_tr_b16 v[122:123], v202 offset:0x2000
	ds_read_b64_tr_b16 v[124:125], v202 offset:0x2800
	ds_read_b64_tr_b16 v[126:127], v202 offset:0x3000
	ds_read_b64_tr_b16 v[128:129], v202 offset:0x3800
	s_waitcnt lgkmcnt(0)
	s_nop 0
	v_mfma_f32_32x32x16_bf16 v[0:15], v[98:101], v[114:117], v[0:15]
	ds_read_b64_tr_b16 v[114:115], v202 offset:0x200
	ds_read_b64_tr_b16 v[116:117], v202 offset:0xa00
	v_mfma_f32_32x32x16_bf16 v[0:15], v[102:105], v[118:121], v[0:15]
	ds_read_b64_tr_b16 v[118:119], v202 offset:0x1200
	ds_read_b64_tr_b16 v[120:121], v202 offset:0x1a00
	v_mfma_f32_32x32x16_bf16 v[0:15], v[106:109], v[122:125], v[0:15]
	ds_read_b64_tr_b16 v[122:123], v202 offset:0x2200
	ds_read_b64_tr_b16 v[124:125], v202 offset:0x2a00
	v_mfma_f32_32x32x16_bf16 v[0:15], v[110:113], v[126:129], v[0:15]
	ds_read_b64_tr_b16 v[126:127], v202 offset:0x3200
	ds_read_b64_tr_b16 v[128:129], v202 offset:0x3a00
	s_waitcnt lgkmcnt(0)
	v_mfma_f32_32x32x16_bf16 v[48:63], v[98:101], v[114:117], v[48:63]
	ds_read_b64_tr_b16 v[114:115], v202 offset:0x400
	ds_read_b64_tr_b16 v[116:117], v202 offset:0xc00
	v_mfma_f32_32x32x16_bf16 v[48:63], v[102:105], v[118:121], v[48:63]
	ds_read_b64_tr_b16 v[118:119], v202 offset:0x1400
	ds_read_b64_tr_b16 v[120:121], v202 offset:0x1c00
	v_mfma_f32_32x32x16_bf16 v[48:63], v[106:109], v[122:125], v[48:63]
	ds_read_b64_tr_b16 v[122:123], v202 offset:0x2400
	ds_read_b64_tr_b16 v[124:125], v202 offset:0x2c00
	v_mfma_f32_32x32x16_bf16 v[48:63], v[110:113], v[126:129], v[48:63]
	ds_read_b64_tr_b16 v[126:127], v202 offset:0x3400
	ds_read_b64_tr_b16 v[128:129], v202 offset:0x3c00
	s_waitcnt lgkmcnt(0)
	v_mfma_f32_32x32x16_bf16 v[32:47], v[98:101], v[114:117], v[32:47]
	ds_read_b64_tr_b16 v[114:115], v202 offset:0x600
	ds_read_b64_tr_b16 v[116:117], v202 offset:0xe00
	v_mfma_f32_32x32x16_bf16 v[32:47], v[102:105], v[118:121], v[32:47]
	ds_read_b64_tr_b16 v[118:119], v202 offset:0x1600
	ds_read_b64_tr_b16 v[120:121], v202 offset:0x1e00
	v_mfma_f32_32x32x16_bf16 v[32:47], v[106:109], v[122:125], v[32:47]
	ds_read_b64_tr_b16 v[122:123], v202 offset:0x2600
	ds_read_b64_tr_b16 v[124:125], v202 offset:0x2e00
	v_mfma_f32_32x32x16_bf16 v[32:47], v[110:113], v[126:129], v[32:47]
	ds_read_b64_tr_b16 v[126:127], v202 offset:0x3600
	ds_read_b64_tr_b16 v[128:129], v202 offset:0x3e00
	s_waitcnt lgkmcnt(0)
	v_mfma_f32_32x32x16_bf16 v[16:31], v[98:101], v[114:117], v[16:31]
	v_max_f32_e32 v98, v81, v81
	v_max_f32_e32 v99, v80, v80
	v_max_f32_e32 v98, v99, v98
	v_max3_f32 v98, v98, v82, v83
	v_max3_f32 v98, v98, v84, v85
	v_max3_f32 v98, v98, v86, v87
	v_max3_f32 v98, v98, v88, v89
	v_max3_f32 v98, v98, v90, v91
	v_max3_f32 v98, v98, v92, v93
	v_mfma_f32_32x32x16_bf16 v[16:31], v[102:105], v[118:121], v[16:31]
	v_max3_f32 v98, v98, v94, v95
	v_max3_f32 v98, v98, v64, v65
	v_max3_f32 v98, v98, v66, v67
	v_max3_f32 v98, v98, v68, v69
	v_max3_f32 v98, v98, v70, v71
	v_max3_f32 v98, v98, v72, v73
	v_max3_f32 v98, v98, v74, v75
	v_max3_f32 v98, v98, v76, v77
	v_mfma_f32_32x32x16_bf16 v[16:31], v[106:109], v[122:125], v[16:31]
	v_max3_f32 v98, v98, v78, v79
	v_mov_b32_e32 v99, v98
	s_nop 1
	v_permlane32_swap_b32_e32 v98, v99
	v_max_f32_e32 v99, v99, v99
	v_max_f32_e32 v98, v98, v98
	v_max_f32_e32 v98, v98, v99
	v_sub_f32_e32 v99, v98, v222
	s_mov_b32 s0, 0x42b504f3
	v_cmp_ge_f32_e32 vcc, s0, v99
	v_max_f32_e32 v99, v222, v222
	v_max_f32_e32 v99, v99, v98
	v_mfma_f32_32x32x16_bf16 v[16:31], v[110:113], v[126:129], v[16:31]
	v_sub_f32_e32 v98, v222, v99
	v_mul_f32_e32 v98, 0x3e0293ee, v98
	v_exp_f32_e32 v98, v98
	s_cmp_eq_u64 vcc, exec
	s_cselect_b64 s[0:1], -1, 0
	v_cndmask_b32_e64 v98, v98, 1.0, s[0:1]
	v_cmp_gt_f32_e32 vcc, 1.0, v98
	s_barrier
	s_cbranch_vccz .LBB0_628
	s_and_saveexec_b64 s[2:3], s[4:5]
	v_readlane_b32 s72, v254, 57
	s_movk_i32 s66, 0x2400
	s_movk_i32 s67, 0xffe0
	s_movk_i32 s68, 0x1200
	v_readlane_b32 s73, v254, 58
	v_readlane_b32 s34, v254, 55
	v_readlane_b32 s35, v254, 56
	v_readlane_b32 s74, v254, 59
	v_readlane_b32 s75, v254, 60
	v_readlane_b32 s76, v254, 61
	v_readlane_b32 s77, v254, 62
	v_readlane_b32 s78, v254, 63
	v_readlane_b32 s79, v255, 0
	v_readlane_b32 s80, v255, 1
	v_readlane_b32 s81, v255, 2
	v_readlane_b32 s82, v255, 3
	v_readlane_b32 s83, v255, 4
	v_readlane_b32 s84, v255, 5
	v_readlane_b32 s85, v255, 6
	v_readlane_b32 s86, v255, 7
	v_readlane_b32 s87, v255, 8
	ds_write_b32 v171, v98 offset:128
	s_or_b64 exec, exec, s[2:3]
	s_waitcnt lgkmcnt(0)
	v_add_u32_e32 v112, v159, v148
	ds_read_b128 v[100:103], v112 offset:224
	ds_read_b128 v[104:107], v112 offset:192
	ds_read_b128 v[108:111], v112 offset:160
	ds_read_b128 v[112:115], v112 offset:128
	s_waitcnt lgkmcnt(3)
	v_pk_mul_f32 v[12:13], v[12:13], v[100:101]
	s_waitcnt lgkmcnt(2)
	v_pk_mul_f32 v[8:9], v[8:9], v[104:105]
	s_waitcnt lgkmcnt(1)
	v_pk_mul_f32 v[4:5], v[4:5], v[108:109]
	v_pk_mul_f32 v[14:15], v[14:15], v[102:103]
	v_pk_mul_f32 v[10:11], v[10:11], v[106:107]
	v_pk_mul_f32 v[6:7], v[6:7], v[110:111]
	s_waitcnt lgkmcnt(0)
	v_pk_mul_f32 v[2:3], v[2:3], v[114:115]
	v_pk_mul_f32 v[0:1], v[0:1], v[112:113]
	v_pk_mul_f32 v[60:61], v[60:61], v[100:101]
	v_pk_mul_f32 v[56:57], v[56:57], v[104:105]
	v_pk_mul_f32 v[52:53], v[52:53], v[108:109]
	v_pk_mul_f32 v[62:63], v[62:63], v[102:103]
	v_pk_mul_f32 v[58:59], v[58:59], v[106:107]
	v_pk_mul_f32 v[54:55], v[54:55], v[110:111]
	v_pk_mul_f32 v[50:51], v[50:51], v[114:115]
	v_pk_mul_f32 v[48:49], v[48:49], v[112:113]
	v_pk_mul_f32 v[44:45], v[44:45], v[100:101]
	v_pk_mul_f32 v[40:41], v[40:41], v[104:105]
	v_pk_mul_f32 v[36:37], v[36:37], v[108:109]
	v_pk_mul_f32 v[46:47], v[46:47], v[102:103]
	v_pk_mul_f32 v[42:43], v[42:43], v[106:107]
	v_pk_mul_f32 v[38:39], v[38:39], v[110:111]
	v_pk_mul_f32 v[34:35], v[34:35], v[114:115]
	v_pk_mul_f32 v[32:33], v[32:33], v[112:113]
	v_pk_mul_f32 v[28:29], v[28:29], v[100:101]
	v_pk_mul_f32 v[24:25], v[24:25], v[104:105]
	v_pk_mul_f32 v[20:21], v[20:21], v[108:109]
	v_pk_mul_f32 v[30:31], v[30:31], v[102:103]
	v_pk_mul_f32 v[26:27], v[26:27], v[106:107]
	v_pk_mul_f32 v[22:23], v[22:23], v[110:111]
	v_pk_mul_f32 v[18:19], v[18:19], v[114:115]
	v_pk_mul_f32 v[16:17], v[16:17], v[112:113]
	s_branch .LBB0_629
